# v22 + write-through (sc1 nt) stores for converted weights
# speedup vs baseline: 1.0050x; 1.0050x over previous
.LBB0_58:
	v_mad_i64_i32 v[88:89], s[22:23], v89, s21, 0
	v_lshl_add_u64 v[88:89], v[88:89], 1, s[18:19]
	v_lshl_add_u64 v[88:89], s[16:17], 1, v[88:89]
	v_lshl_add_u64 v[88:89], v[88:89], 0, v[72:73]
	s_waitcnt lgkmcnt(0)
	global_store_dwordx4 v[88:89], v[66:69], off sc1 nt

.LBB0_111:
	v_mov_b64_e32 v[90:91], s[18:19]
	v_mad_i64_i32 v[88:89], s[28:29], v88, s21, v[90:91]
	s_ashr_i32 s17, s16, 31
	v_lshl_add_u64 v[88:89], v[88:89], 0, s[16:17]
	v_lshl_add_u64 v[88:89], v[88:89], 0, v[70:71]
	s_waitcnt lgkmcnt(0)
	global_store_dwordx4 v[88:89], v[66:69], off sc1 nt
	ds_read_b128 v[66:69], v86 offset:16896
	s_cmp_lt_i32 s23, 1
	v_add_u32_e32 v88, 32, v72
	s_cbranch_scc1 .LBB0_115
	s_cmp_eq_u32 s23, 1
	s_mov_b64 s[28:29], -1
	s_cbranch_scc0 .LBB0_114
	v_lshlrev_b32_e32 v89, 2, v88
	v_lshrrev_b32_e32 v90, 1, v88
	v_and_b32_e32 v89, 16, v89
	v_and_b32_e32 v90, 12, v90
	v_and_b32_e32 v91, 0xffffffe3, v88
	v_or3_b32 v89, v89, v91, v90
	s_mov_b64 s[28:29], 0

.LBB0_119:
	v_mov_b64_e32 v[90:91], s[18:19]
	v_mad_i64_i32 v[88:89], s[28:29], v89, s21, v[90:91]
	v_lshl_add_u64 v[88:89], v[88:89], 0, s[16:17]
	v_lshl_add_u64 v[88:89], v[88:89], 0, v[70:71]
	s_waitcnt lgkmcnt(0)
	global_store_dwordx4 v[88:89], v[66:69], off sc1 nt
	ds_read_b128 v[66:69], v86 offset:33792
	s_cmp_lt_i32 s23, 1
	v_add_u32_e32 v88, s24, v80
	s_cbranch_scc1 .LBB0_123
	s_cmp_eq_u32 s23, 1
	s_mov_b64 s[28:29], -1
	s_cbranch_scc0 .LBB0_122
	v_lshlrev_b32_e32 v89, 2, v88
	v_lshrrev_b32_e32 v90, 1, v88
	v_and_b32_e32 v89, 16, v89
	v_and_b32_e32 v90, 12, v90
	v_and_b32_e32 v91, 0xffffffe3, v88
	v_or3_b32 v89, v89, v91, v90
	s_mov_b64 s[28:29], 0

.LBB0_127:
	v_mov_b64_e32 v[90:91], s[18:19]
	v_mad_i64_i32 v[88:89], s[28:29], v89, s21, v[90:91]
	v_lshl_add_u64 v[88:89], v[88:89], 0, s[16:17]
	v_lshl_add_u64 v[88:89], v[88:89], 0, v[70:71]
	s_waitcnt lgkmcnt(0)
	global_store_dwordx4 v[88:89], v[66:69], off sc1 nt
	ds_read_b128 v[66:69], v86 offset:50688
	s_cmp_lt_i32 s23, 1
	v_add_u32_e32 v72, 0x60, v72
	s_cbranch_scc1 .LBB0_131
	s_cmp_eq_u32 s23, 1
	s_mov_b64 s[28:29], -1
	s_cbranch_scc0 .LBB0_130
	v_lshlrev_b32_e32 v88, 2, v72
	v_lshrrev_b32_e32 v89, 1, v72
	v_and_b32_e32 v88, 16, v88
	v_and_b32_e32 v89, 12, v89
	v_and_b32_e32 v90, 0xffffffe3, v72
	v_or3_b32 v88, v88, v90, v89
	s_mov_b64 s[28:29], 0

.LBB0_135:
	v_mov_b64_e32 v[90:91], s[18:19]
	v_mad_i64_i32 v[88:89], s[28:29], v88, s21, v[90:91]
	v_lshl_add_u64 v[88:89], v[88:89], 0, s[16:17]
	v_lshl_add_u64 v[88:89], v[88:89], 0, v[70:71]
	s_waitcnt lgkmcnt(0)
	global_store_dwordx4 v[88:89], v[66:69], off sc1 nt
	s_branch .LBB0_59

.LBB0_144:
	v_mad_i64_i32 v[90:91], s[28:29], v72, s21, 0
	v_lshl_add_u64 v[90:91], v[90:91], 1, s[18:19]
	s_ashr_i32 s17, s16, 31
	v_lshl_add_u64 v[90:91], s[16:17], 1, v[90:91]
	v_lshlrev_b32_e32 v72, 1, v74
	v_lshl_add_u64 v[90:91], v[90:91], 0, v[72:73]
	s_waitcnt lgkmcnt(0)
	global_store_dwordx4 v[90:91], v[66:69], off sc1 nt
	ds_read_b128 v[66:69], v87 offset:8448
	s_cmp_lt_i32 s23, 1
	v_add_u32_e32 v89, 16, v88
	s_cbranch_scc1 .LBB0_148
	s_cmp_eq_u32 s23, 1
	s_mov_b64 s[28:29], -1
	s_cbranch_scc0 .LBB0_147
	v_lshlrev_b32_e32 v90, 2, v89
	v_lshrrev_b32_e32 v91, 1, v89
	v_and_b32_e32 v90, 16, v90
	v_and_b32_e32 v91, 12, v91
	v_and_b32_e32 v92, 0xffffffe3, v89
	v_or3_b32 v90, v90, v92, v91
	s_mov_b64 s[28:29], 0

.LBB0_152:
	v_mad_i64_i32 v[90:91], s[28:29], v90, s21, 0
	v_lshl_add_u64 v[90:91], v[90:91], 1, s[18:19]
	v_lshl_add_u64 v[90:91], s[16:17], 1, v[90:91]
	v_lshl_add_u64 v[90:91], v[90:91], 0, v[72:73]
	s_waitcnt lgkmcnt(0)
	global_store_dwordx4 v[90:91], v[66:69], off sc1 nt
	ds_read_b128 v[66:69], v87 offset:16896
	s_cmp_lt_i32 s23, 1
	v_add_u32_e32 v89, s24, v81
	s_cbranch_scc1 .LBB0_156
	s_cmp_eq_u32 s23, 1
	s_mov_b64 s[28:29], -1
	s_cbranch_scc0 .LBB0_155
	v_lshlrev_b32_e32 v90, 2, v89
	v_lshrrev_b32_e32 v91, 1, v89
	v_and_b32_e32 v90, 16, v90
	v_and_b32_e32 v91, 12, v91
	v_and_b32_e32 v92, 0xffffffe3, v89
	v_or3_b32 v90, v90, v92, v91
	s_mov_b64 s[28:29], 0

.LBB0_160:
	v_mad_i64_i32 v[90:91], s[28:29], v90, s21, 0
	v_lshl_add_u64 v[90:91], v[90:91], 1, s[18:19]
	v_lshl_add_u64 v[90:91], s[16:17], 1, v[90:91]
	v_lshl_add_u64 v[90:91], v[90:91], 0, v[72:73]
	s_waitcnt lgkmcnt(0)
	global_store_dwordx4 v[90:91], v[66:69], off sc1 nt
	ds_read_b128 v[66:69], v87 offset:25344
	s_cmp_lt_i32 s23, 1
	v_add_u32_e32 v89, 48, v88
	s_cbranch_scc1 .LBB0_164
	s_cmp_eq_u32 s23, 1
	s_mov_b64 s[28:29], -1
	s_cbranch_scc0 .LBB0_163
	v_lshlrev_b32_e32 v90, 2, v89
	v_lshrrev_b32_e32 v91, 1, v89
	v_and_b32_e32 v90, 16, v90
	v_and_b32_e32 v91, 12, v91
	v_and_b32_e32 v92, 0xffffffe3, v89
	v_or3_b32 v90, v90, v92, v91
	s_mov_b64 s[28:29], 0

.LBB0_168:
	v_mad_i64_i32 v[90:91], s[28:29], v90, s21, 0
	v_lshl_add_u64 v[90:91], v[90:91], 1, s[18:19]
	v_lshl_add_u64 v[90:91], s[16:17], 1, v[90:91]
	v_lshl_add_u64 v[90:91], v[90:91], 0, v[72:73]
	s_waitcnt lgkmcnt(0)
	global_store_dwordx4 v[90:91], v[66:69], off sc1 nt
	ds_read_b128 v[66:69], v87 offset:33792
	s_cmp_lt_i32 s23, 1
	v_add_u32_e32 v89, s24, v82
	s_cbranch_scc1 .LBB0_172
	s_cmp_eq_u32 s23, 1
	s_mov_b64 s[28:29], -1
	s_cbranch_scc0 .LBB0_171
	v_lshlrev_b32_e32 v90, 2, v89
	v_lshrrev_b32_e32 v91, 1, v89
	v_and_b32_e32 v90, 16, v90
	v_and_b32_e32 v91, 12, v91
	v_and_b32_e32 v92, 0xffffffe3, v89
	v_or3_b32 v90, v90, v92, v91
	s_mov_b64 s[28:29], 0

.LBB0_176:
	v_mad_i64_i32 v[90:91], s[28:29], v90, s21, 0
	v_lshl_add_u64 v[90:91], v[90:91], 1, s[18:19]
	v_lshl_add_u64 v[90:91], s[16:17], 1, v[90:91]
	v_lshl_add_u64 v[90:91], v[90:91], 0, v[72:73]
	s_waitcnt lgkmcnt(0)
	global_store_dwordx4 v[90:91], v[66:69], off sc1 nt
	ds_read_b128 v[66:69], v87 offset:42240
	s_cmp_lt_i32 s23, 1
	v_add_u32_e32 v89, 0x50, v88
	s_cbranch_scc1 .LBB0_180
	s_cmp_eq_u32 s23, 1
	s_mov_b64 s[28:29], -1
	s_cbranch_scc0 .LBB0_179
	v_lshlrev_b32_e32 v90, 2, v89
	v_lshrrev_b32_e32 v91, 1, v89
	v_and_b32_e32 v90, 16, v90
	v_and_b32_e32 v91, 12, v91
	v_and_b32_e32 v92, 0xffffffe3, v89
	v_or3_b32 v90, v90, v92, v91
	s_mov_b64 s[28:29], 0

.LBB0_184:
	v_mad_i64_i32 v[90:91], s[28:29], v90, s21, 0
	v_lshl_add_u64 v[90:91], v[90:91], 1, s[18:19]
	v_lshl_add_u64 v[90:91], s[16:17], 1, v[90:91]
	v_lshl_add_u64 v[90:91], v[90:91], 0, v[72:73]
	s_waitcnt lgkmcnt(0)
	global_store_dwordx4 v[90:91], v[66:69], off sc1 nt
	ds_read_b128 v[66:69], v87 offset:50688
	s_cmp_lt_i32 s23, 1
	v_add_u32_e32 v89, s24, v83
	s_cbranch_scc1 .LBB0_188
	s_cmp_eq_u32 s23, 1
	s_mov_b64 s[28:29], -1
	s_cbranch_scc0 .LBB0_187
	v_lshlrev_b32_e32 v90, 2, v89
	v_lshrrev_b32_e32 v91, 1, v89
	v_and_b32_e32 v90, 16, v90
	v_and_b32_e32 v91, 12, v91
	v_and_b32_e32 v92, 0xffffffe3, v89
	v_or3_b32 v90, v90, v92, v91
	s_mov_b64 s[28:29], 0

.LBB0_192:
	v_mad_i64_i32 v[90:91], s[28:29], v90, s21, 0
	v_lshl_add_u64 v[90:91], v[90:91], 1, s[18:19]
	v_lshl_add_u64 v[90:91], s[16:17], 1, v[90:91]
	v_lshl_add_u64 v[90:91], v[90:91], 0, v[72:73]
	s_waitcnt lgkmcnt(0)
	global_store_dwordx4 v[90:91], v[66:69], off sc1 nt
	ds_read_b128 v[66:69], v87 offset:59136
	s_cmp_lt_i32 s23, 1
	v_add_u32_e32 v88, 0x70, v88
	s_cbranch_scc1 .LBB0_196
	s_cmp_eq_u32 s23, 1
	s_mov_b64 s[28:29], -1
	s_cbranch_scc0 .LBB0_195
	v_lshlrev_b32_e32 v89, 2, v88
	v_lshrrev_b32_e32 v90, 1, v88
	v_and_b32_e32 v89, 16, v89
	v_and_b32_e32 v90, 12, v90
	v_and_b32_e32 v91, 0xffffffe3, v88
	v_or3_b32 v89, v89, v91, v90
	s_mov_b64 s[28:29], 0

.LBB0_536:
	v_mad_i64_i32 v[82:83], s[22:23], v79, s68, 0
	v_lshl_add_u64 v[82:83], v[82:83], 1, s[80:81]
	v_lshl_add_u64 v[82:83], s[78:79], 1, v[82:83]
	v_lshl_add_u64 v[82:83], v[82:83], 0, v[74:75]
	s_waitcnt lgkmcnt(0)
	global_store_dwordx4 v[82:83], v[66:69], off sc1 nt

.LBB0_601:
	v_mov_b64_e32 v[82:83], s[80:81]
	v_mad_i64_i32 v[82:83], s[22:23], v79, s68, v[82:83]
	s_ashr_i32 s79, s78, 31
	v_lshl_add_u64 v[82:83], v[82:83], 0, s[78:79]
	v_lshl_add_u64 v[82:83], v[82:83], 0, v[178:179]
	s_waitcnt lgkmcnt(0)
	global_store_dwordx4 v[82:83], v[66:69], off sc1 nt
	ds_read_b128 v[66:69], v74 offset:16896
	s_cmp_lt_i32 s12, 1
	v_add_u32_e32 v77, s10, v194
	s_cbranch_scc1 .LBB0_605
	s_cmp_eq_u32 s12, 1
	s_mov_b64 s[28:29], -1
	s_cbranch_scc0 .LBB0_604
	v_lshlrev_b32_e32 v79, 2, v77
	v_lshrrev_b32_e32 v82, 1, v77
	v_and_b32_e32 v79, 16, v79
	v_and_b32_e32 v82, 12, v82
	v_and_b32_e32 v83, 0xffffffe3, v77
	v_or3_b32 v79, v79, v83, v82
	s_mov_b64 s[28:29], 0

.LBB0_609:
	v_mov_b64_e32 v[82:83], s[80:81]
	v_mad_i64_i32 v[82:83], s[22:23], v79, s68, v[82:83]
	v_lshl_add_u64 v[82:83], v[82:83], 0, s[78:79]
	v_lshl_add_u64 v[82:83], v[82:83], 0, v[178:179]
	s_waitcnt lgkmcnt(0)
	global_store_dwordx4 v[82:83], v[66:69], off sc1 nt
	ds_read_b128 v[66:69], v74 offset:33792
	s_cmp_lt_i32 s12, 1
	v_add_u32_e32 v77, s10, v202
	s_cbranch_scc1 .LBB0_613
	s_cmp_eq_u32 s12, 1
	s_mov_b64 s[28:29], -1
	s_cbranch_scc0 .LBB0_612
	v_lshlrev_b32_e32 v79, 2, v77
	v_lshrrev_b32_e32 v82, 1, v77
	v_and_b32_e32 v79, 16, v79
	v_and_b32_e32 v82, 12, v82
	v_and_b32_e32 v83, 0xffffffe3, v77
	v_or3_b32 v79, v79, v83, v82
	s_mov_b64 s[28:29], 0

.LBB0_617:
	v_mov_b64_e32 v[82:83], s[80:81]
	v_mad_i64_i32 v[82:83], s[22:23], v79, s68, v[82:83]
	v_lshl_add_u64 v[82:83], v[82:83], 0, s[78:79]
	v_lshl_add_u64 v[82:83], v[82:83], 0, v[178:179]
	s_waitcnt lgkmcnt(0)
	global_store_dwordx4 v[82:83], v[66:69], off sc1 nt
	ds_read_b128 v[66:69], v74 offset:50688
	s_cmp_lt_i32 s12, 1
	v_add_u32_e32 v74, s10, v203
	s_cbranch_scc1 .LBB0_621
	s_cmp_eq_u32 s12, 1
	s_mov_b64 s[28:29], -1
	s_cbranch_scc0 .LBB0_620
	v_lshlrev_b32_e32 v77, 2, v74
	v_lshrrev_b32_e32 v79, 1, v74
	v_and_b32_e32 v77, 16, v77
	v_and_b32_e32 v79, 12, v79
	v_and_b32_e32 v82, 0xffffffe3, v74
	v_or3_b32 v77, v77, v82, v79
	s_mov_b64 s[28:29], 0

.LBB0_625:
	v_mov_b64_e32 v[82:83], s[80:81]
	v_mad_i64_i32 v[82:83], s[22:23], v77, s68, v[82:83]
	v_lshl_add_u64 v[82:83], v[82:83], 0, s[78:79]
	v_lshl_add_u64 v[82:83], v[82:83], 0, v[178:179]
	s_waitcnt lgkmcnt(0)
	global_store_dwordx4 v[82:83], v[66:69], off sc1 nt
	s_branch .LBB0_537

.LBB0_634:
	v_mad_i64_i32 v[82:83], s[22:23], v79, s68, 0
	v_lshl_add_u64 v[82:83], v[82:83], 1, s[80:81]
	s_ashr_i32 s79, s78, 31
	v_lshl_add_u64 v[82:83], s[78:79], 1, v[82:83]
	v_lshlrev_b32_e32 v74, 1, v195
	v_lshl_add_u64 v[82:83], v[82:83], 0, v[74:75]
	s_waitcnt lgkmcnt(0)
	global_store_dwordx4 v[82:83], v[66:69], off sc1 nt
	ds_read_b128 v[66:69], v77 offset:8448
	s_cmp_lt_i32 s12, 1
	v_add_u32_e32 v79, s10, v213
	s_cbranch_scc1 .LBB0_638
	s_cmp_eq_u32 s12, 1
	s_mov_b64 s[28:29], -1
	s_cbranch_scc0 .LBB0_637
	v_lshlrev_b32_e32 v82, 2, v79
	v_lshrrev_b32_e32 v83, 1, v79
	v_and_b32_e32 v82, 16, v82
	v_and_b32_e32 v83, 12, v83
	v_and_b32_e32 v85, 0xffffffe3, v79
	v_or3_b32 v82, v82, v85, v83
	s_mov_b64 s[28:29], 0

.LBB0_642:
	v_mad_i64_i32 v[82:83], s[22:23], v82, s68, 0
	v_lshl_add_u64 v[82:83], v[82:83], 1, s[80:81]
	v_lshl_add_u64 v[82:83], s[78:79], 1, v[82:83]
	v_lshl_add_u64 v[82:83], v[82:83], 0, v[74:75]
	s_waitcnt lgkmcnt(0)
	global_store_dwordx4 v[82:83], v[66:69], off sc1 nt
	ds_read_b128 v[66:69], v77 offset:16896
	s_cmp_lt_i32 s12, 1
	v_add_u32_e32 v79, s10, v209
	s_cbranch_scc1 .LBB0_646
	s_cmp_eq_u32 s12, 1
	s_mov_b64 s[28:29], -1
	s_cbranch_scc0 .LBB0_645
	v_lshlrev_b32_e32 v82, 2, v79
	v_lshrrev_b32_e32 v83, 1, v79
	v_and_b32_e32 v82, 16, v82
	v_and_b32_e32 v83, 12, v83
	v_and_b32_e32 v85, 0xffffffe3, v79
	v_or3_b32 v82, v82, v85, v83
	s_mov_b64 s[28:29], 0

.LBB0_650:
	v_mad_i64_i32 v[82:83], s[22:23], v82, s68, 0
	v_lshl_add_u64 v[82:83], v[82:83], 1, s[80:81]
	v_lshl_add_u64 v[82:83], s[78:79], 1, v[82:83]
	v_lshl_add_u64 v[82:83], v[82:83], 0, v[74:75]
	s_waitcnt lgkmcnt(0)
	global_store_dwordx4 v[82:83], v[66:69], off sc1 nt
	ds_read_b128 v[66:69], v77 offset:25344
	s_cmp_lt_i32 s12, 1
	v_add_u32_e32 v79, s10, v208
	s_cbranch_scc1 .LBB0_654
	s_cmp_eq_u32 s12, 1
	s_mov_b64 s[28:29], -1
	s_cbranch_scc0 .LBB0_653
	v_lshlrev_b32_e32 v82, 2, v79
	v_lshrrev_b32_e32 v83, 1, v79
	v_and_b32_e32 v82, 16, v82
	v_and_b32_e32 v83, 12, v83
	v_and_b32_e32 v85, 0xffffffe3, v79
	v_or3_b32 v82, v82, v85, v83
	s_mov_b64 s[28:29], 0

.LBB0_658:
	v_mad_i64_i32 v[82:83], s[22:23], v82, s68, 0
	v_lshl_add_u64 v[82:83], v[82:83], 1, s[80:81]
	v_lshl_add_u64 v[82:83], s[78:79], 1, v[82:83]
	v_lshl_add_u64 v[82:83], v[82:83], 0, v[74:75]
	s_waitcnt lgkmcnt(0)
	global_store_dwordx4 v[82:83], v[66:69], off sc1 nt
	ds_read_b128 v[66:69], v77 offset:33792
	s_cmp_lt_i32 s12, 1
	v_add_u32_e32 v79, s10, v211
	s_cbranch_scc1 .LBB0_662
	s_cmp_eq_u32 s12, 1
	s_mov_b64 s[28:29], -1
	s_cbranch_scc0 .LBB0_661
	v_lshlrev_b32_e32 v82, 2, v79
	v_lshrrev_b32_e32 v83, 1, v79
	v_and_b32_e32 v82, 16, v82
	v_and_b32_e32 v83, 12, v83
	v_and_b32_e32 v85, 0xffffffe3, v79
	v_or3_b32 v82, v82, v85, v83
	s_mov_b64 s[28:29], 0

.LBB0_666:
	v_mad_i64_i32 v[82:83], s[22:23], v82, s68, 0
	v_lshl_add_u64 v[82:83], v[82:83], 1, s[80:81]
	v_lshl_add_u64 v[82:83], s[78:79], 1, v[82:83]
	v_lshl_add_u64 v[82:83], v[82:83], 0, v[74:75]
	s_waitcnt lgkmcnt(0)
	global_store_dwordx4 v[82:83], v[66:69], off sc1 nt
	ds_read_b128 v[66:69], v77 offset:42240
	s_cmp_lt_i32 s12, 1
	v_add_u32_e32 v79, s10, v210
	s_cbranch_scc1 .LBB0_670
	s_cmp_eq_u32 s12, 1
	s_mov_b64 s[28:29], -1
	s_cbranch_scc0 .LBB0_669
	v_lshlrev_b32_e32 v82, 2, v79
	v_lshrrev_b32_e32 v83, 1, v79
	v_and_b32_e32 v82, 16, v82
	v_and_b32_e32 v83, 12, v83
	v_and_b32_e32 v85, 0xffffffe3, v79
	v_or3_b32 v82, v82, v85, v83
	s_mov_b64 s[28:29], 0

.LBB0_674:
	v_mad_i64_i32 v[82:83], s[22:23], v82, s68, 0
	v_lshl_add_u64 v[82:83], v[82:83], 1, s[80:81]
	v_lshl_add_u64 v[82:83], s[78:79], 1, v[82:83]
	v_lshl_add_u64 v[82:83], v[82:83], 0, v[74:75]
	s_waitcnt lgkmcnt(0)
	global_store_dwordx4 v[82:83], v[66:69], off sc1 nt
	ds_read_b128 v[66:69], v77 offset:50688
	s_cmp_lt_i32 s12, 1
	v_add_u32_e32 v79, s10, v90
	s_cbranch_scc1 .LBB0_678
	s_cmp_eq_u32 s12, 1
	s_mov_b64 s[28:29], -1
	s_cbranch_scc0 .LBB0_677
	v_lshlrev_b32_e32 v82, 2, v79
	v_lshrrev_b32_e32 v83, 1, v79
	v_and_b32_e32 v82, 16, v82
	v_and_b32_e32 v83, 12, v83
	v_and_b32_e32 v85, 0xffffffe3, v79
	v_or3_b32 v82, v82, v85, v83
	s_mov_b64 s[28:29], 0

.LBB0_682:
	v_mad_i64_i32 v[82:83], s[22:23], v82, s68, 0
	v_lshl_add_u64 v[82:83], v[82:83], 1, s[80:81]
	v_lshl_add_u64 v[82:83], s[78:79], 1, v[82:83]
	v_lshl_add_u64 v[82:83], v[82:83], 0, v[74:75]
	s_waitcnt lgkmcnt(0)
	global_store_dwordx4 v[82:83], v[66:69], off sc1 nt
	ds_read_b128 v[66:69], v77 offset:59136
	s_cmp_lt_i32 s12, 1
	v_add_u32_e32 v77, s10, v212
	s_cbranch_scc1 .LBB0_686
	s_cmp_eq_u32 s12, 1
	s_mov_b64 s[28:29], -1
	s_cbranch_scc0 .LBB0_685
	v_lshlrev_b32_e32 v79, 2, v77
	v_lshrrev_b32_e32 v82, 1, v77
	v_and_b32_e32 v79, 16, v79
	v_and_b32_e32 v82, 12, v82
	v_and_b32_e32 v83, 0xffffffe3, v77
	v_or3_b32 v79, v79, v83, v82
	s_mov_b64 s[28:29], 0

.LBB0_777:
	v_mad_i64_i32 v[74:75], s[22:23], v74, s66, 0
	v_lshl_add_u64 v[74:75], v[74:75], 1, s[78:79]
	v_lshl_add_u64 v[74:75], s[74:75], 1, v[74:75]
	v_lshl_add_u64 v[74:75], v[74:75], 0, v[70:71]
	s_waitcnt lgkmcnt(0)
	global_store_dwordx4 v[74:75], v[66:69], off sc1 nt

.LBB0_842:
	v_mov_b64_e32 v[76:77], s[78:79]
	v_mad_i64_i32 v[74:75], s[22:23], v74, s66, v[76:77]
	s_ashr_i32 s75, s74, 31
	v_lshl_add_u64 v[74:75], v[74:75], 0, s[74:75]
	v_lshl_add_u64 v[74:75], v[74:75], 0, v[178:179]
	s_waitcnt lgkmcnt(0)
	global_store_dwordx4 v[74:75], v[66:69], off sc1 nt
	ds_read_b128 v[66:69], v70 offset:16896
	s_cmp_lt_i32 s12, 1
	v_add_u32_e32 v73, s10, v194
	s_cbranch_scc1 .LBB0_846
	s_cmp_eq_u32 s12, 1
	s_mov_b64 s[28:29], -1
	s_cbranch_scc0 .LBB0_845
	v_lshlrev_b32_e32 v74, 2, v73
	v_lshrrev_b32_e32 v75, 1, v73
	v_and_b32_e32 v74, 16, v74
	v_and_b32_e32 v75, 12, v75
	v_and_b32_e32 v76, 0xffffffe3, v73
	v_or3_b32 v74, v74, v76, v75
	s_mov_b64 s[28:29], 0

.LBB0_850:
	v_mov_b64_e32 v[76:77], s[78:79]
	v_mad_i64_i32 v[74:75], s[22:23], v74, s66, v[76:77]
	v_lshl_add_u64 v[74:75], v[74:75], 0, s[74:75]
	v_lshl_add_u64 v[74:75], v[74:75], 0, v[178:179]
	s_waitcnt lgkmcnt(0)
	global_store_dwordx4 v[74:75], v[66:69], off sc1 nt
	ds_read_b128 v[66:69], v70 offset:33792
	s_cmp_lt_i32 s12, 1
	v_add_u32_e32 v73, s10, v202
	s_cbranch_scc1 .LBB0_854
	s_cmp_eq_u32 s12, 1
	s_mov_b64 s[28:29], -1
	s_cbranch_scc0 .LBB0_853
	v_lshlrev_b32_e32 v74, 2, v73
	v_lshrrev_b32_e32 v75, 1, v73
	v_and_b32_e32 v74, 16, v74
	v_and_b32_e32 v75, 12, v75
	v_and_b32_e32 v76, 0xffffffe3, v73
	v_or3_b32 v74, v74, v76, v75
	s_mov_b64 s[28:29], 0

.LBB0_858:
	v_mov_b64_e32 v[76:77], s[78:79]
	v_mad_i64_i32 v[74:75], s[22:23], v74, s66, v[76:77]
	v_lshl_add_u64 v[74:75], v[74:75], 0, s[74:75]
	v_lshl_add_u64 v[74:75], v[74:75], 0, v[178:179]
	s_waitcnt lgkmcnt(0)
	global_store_dwordx4 v[74:75], v[66:69], off sc1 nt
	ds_read_b128 v[66:69], v70 offset:50688
	s_cmp_lt_i32 s12, 1
	v_add_u32_e32 v70, s10, v203
	s_cbranch_scc1 .LBB0_862
	s_cmp_eq_u32 s12, 1
	s_mov_b64 s[28:29], -1
	s_cbranch_scc0 .LBB0_861
	v_lshlrev_b32_e32 v73, 2, v70
	v_lshrrev_b32_e32 v74, 1, v70
	v_and_b32_e32 v73, 16, v73
	v_and_b32_e32 v74, 12, v74
	v_and_b32_e32 v75, 0xffffffe3, v70
	v_or3_b32 v73, v73, v75, v74
	s_mov_b64 s[28:29], 0

.LBB0_866:
	v_mov_b64_e32 v[74:75], s[78:79]
	v_mad_i64_i32 v[74:75], s[22:23], v73, s66, v[74:75]
	v_lshl_add_u64 v[74:75], v[74:75], 0, s[74:75]
	v_lshl_add_u64 v[74:75], v[74:75], 0, v[178:179]
	s_waitcnt lgkmcnt(0)
	global_store_dwordx4 v[74:75], v[66:69], off sc1 nt
	s_branch .LBB0_778

.LBB0_875:
	v_mad_i64_i32 v[74:75], s[22:23], v74, s66, 0
	v_lshl_add_u64 v[74:75], v[74:75], 1, s[78:79]
	s_ashr_i32 s75, s74, 31
	v_lshl_add_u64 v[74:75], s[74:75], 1, v[74:75]
	v_lshlrev_b32_e32 v70, 1, v195
	v_lshl_add_u64 v[74:75], v[74:75], 0, v[70:71]
	s_waitcnt lgkmcnt(0)
	global_store_dwordx4 v[74:75], v[66:69], off sc1 nt
	ds_read_b128 v[66:69], v73 offset:8448
	s_cmp_lt_i32 s12, 1
	v_add_u32_e32 v74, s10, v207
	s_cbranch_scc1 .LBB0_879
	s_cmp_eq_u32 s12, 1
	s_mov_b64 s[28:29], -1
	s_cbranch_scc0 .LBB0_878
	v_lshlrev_b32_e32 v75, 2, v74
	v_lshrrev_b32_e32 v76, 1, v74
	v_and_b32_e32 v75, 16, v75
	v_and_b32_e32 v76, 12, v76
	v_and_b32_e32 v77, 0xffffffe3, v74
	v_or3_b32 v75, v75, v77, v76
	s_mov_b64 s[28:29], 0

.LBB0_883:
	v_mad_i64_i32 v[74:75], s[22:23], v75, s66, 0
	v_lshl_add_u64 v[74:75], v[74:75], 1, s[78:79]
	v_lshl_add_u64 v[74:75], s[74:75], 1, v[74:75]
	v_lshl_add_u64 v[74:75], v[74:75], 0, v[70:71]
	s_waitcnt lgkmcnt(0)
	global_store_dwordx4 v[74:75], v[66:69], off sc1 nt
	ds_read_b128 v[66:69], v73 offset:16896
	s_cmp_lt_i32 s12, 1
	v_add_u32_e32 v74, s10, v213
	s_cbranch_scc1 .LBB0_887
	s_cmp_eq_u32 s12, 1
	s_mov_b64 s[28:29], -1
	s_cbranch_scc0 .LBB0_886
	v_lshlrev_b32_e32 v75, 2, v74
	v_lshrrev_b32_e32 v76, 1, v74
	v_and_b32_e32 v75, 16, v75
	v_and_b32_e32 v76, 12, v76
	v_and_b32_e32 v77, 0xffffffe3, v74
	v_or3_b32 v75, v75, v77, v76
	s_mov_b64 s[28:29], 0

.LBB0_891:
	v_mad_i64_i32 v[74:75], s[22:23], v75, s66, 0
	v_lshl_add_u64 v[74:75], v[74:75], 1, s[78:79]
	v_lshl_add_u64 v[74:75], s[74:75], 1, v[74:75]
	v_lshl_add_u64 v[74:75], v[74:75], 0, v[70:71]
	s_waitcnt lgkmcnt(0)
	global_store_dwordx4 v[74:75], v[66:69], off sc1 nt
	ds_read_b128 v[66:69], v73 offset:25344
	s_cmp_lt_i32 s12, 1
	v_add_u32_e32 v74, s10, v208
	s_cbranch_scc1 .LBB0_895
	s_cmp_eq_u32 s12, 1
	s_mov_b64 s[28:29], -1
	s_cbranch_scc0 .LBB0_894
	v_lshlrev_b32_e32 v75, 2, v74
	v_lshrrev_b32_e32 v76, 1, v74
	v_and_b32_e32 v75, 16, v75
	v_and_b32_e32 v76, 12, v76
	v_and_b32_e32 v77, 0xffffffe3, v74
	v_or3_b32 v75, v75, v77, v76
	s_mov_b64 s[28:29], 0

.LBB0_899:
	v_mad_i64_i32 v[74:75], s[22:23], v75, s66, 0
	v_lshl_add_u64 v[74:75], v[74:75], 1, s[78:79]
	v_lshl_add_u64 v[74:75], s[74:75], 1, v[74:75]
	v_lshl_add_u64 v[74:75], v[74:75], 0, v[70:71]
	s_waitcnt lgkmcnt(0)
	global_store_dwordx4 v[74:75], v[66:69], off sc1 nt
	ds_read_b128 v[66:69], v73 offset:33792
	s_cmp_lt_i32 s12, 1
	v_add_u32_e32 v74, s10, v209
	s_cbranch_scc1 .LBB0_903
	s_cmp_eq_u32 s12, 1
	s_mov_b64 s[28:29], -1
	s_cbranch_scc0 .LBB0_902
	v_lshlrev_b32_e32 v75, 2, v74
	v_lshrrev_b32_e32 v76, 1, v74
	v_and_b32_e32 v75, 16, v75
	v_and_b32_e32 v76, 12, v76
	v_and_b32_e32 v77, 0xffffffe3, v74
	v_or3_b32 v75, v75, v77, v76
	s_mov_b64 s[28:29], 0

.LBB0_907:
	v_mad_i64_i32 v[74:75], s[22:23], v75, s66, 0
	v_lshl_add_u64 v[74:75], v[74:75], 1, s[78:79]
	v_lshl_add_u64 v[74:75], s[74:75], 1, v[74:75]
	v_lshl_add_u64 v[74:75], v[74:75], 0, v[70:71]
	s_waitcnt lgkmcnt(0)
	global_store_dwordx4 v[74:75], v[66:69], off sc1 nt
	ds_read_b128 v[66:69], v73 offset:42240
	s_cmp_lt_i32 s12, 1
	v_add_u32_e32 v74, s10, v210
	s_cbranch_scc1 .LBB0_911
	s_cmp_eq_u32 s12, 1
	s_mov_b64 s[28:29], -1
	s_cbranch_scc0 .LBB0_910
	v_lshlrev_b32_e32 v75, 2, v74
	v_lshrrev_b32_e32 v76, 1, v74
	v_and_b32_e32 v75, 16, v75
	v_and_b32_e32 v76, 12, v76
	v_and_b32_e32 v77, 0xffffffe3, v74
	v_or3_b32 v75, v75, v77, v76
	s_mov_b64 s[28:29], 0

.LBB0_915:
	v_mad_i64_i32 v[74:75], s[22:23], v75, s66, 0
	v_lshl_add_u64 v[74:75], v[74:75], 1, s[78:79]
	v_lshl_add_u64 v[74:75], s[74:75], 1, v[74:75]
	v_lshl_add_u64 v[74:75], v[74:75], 0, v[70:71]
	s_waitcnt lgkmcnt(0)
	global_store_dwordx4 v[74:75], v[66:69], off sc1 nt
	ds_read_b128 v[66:69], v73 offset:50688
	s_cmp_lt_i32 s12, 1
	v_add_u32_e32 v74, s10, v211
	s_cbranch_scc1 .LBB0_919
	s_cmp_eq_u32 s12, 1
	s_mov_b64 s[28:29], -1
	s_cbranch_scc0 .LBB0_918
	v_lshlrev_b32_e32 v75, 2, v74
	v_lshrrev_b32_e32 v76, 1, v74
	v_and_b32_e32 v75, 16, v75
	v_and_b32_e32 v76, 12, v76
	v_and_b32_e32 v77, 0xffffffe3, v74
	v_or3_b32 v75, v75, v77, v76
	s_mov_b64 s[28:29], 0

.LBB0_923:
	v_mad_i64_i32 v[74:75], s[22:23], v75, s66, 0
	v_lshl_add_u64 v[74:75], v[74:75], 1, s[78:79]
	v_lshl_add_u64 v[74:75], s[74:75], 1, v[74:75]
	v_lshl_add_u64 v[74:75], v[74:75], 0, v[70:71]
	s_waitcnt lgkmcnt(0)
	global_store_dwordx4 v[74:75], v[66:69], off sc1 nt
	ds_read_b128 v[66:69], v73 offset:59136
	s_cmp_lt_i32 s12, 1
	v_add_u32_e32 v73, s10, v212
	s_cbranch_scc1 .LBB0_927
	s_cmp_eq_u32 s12, 1
	s_mov_b64 s[28:29], -1
	s_cbranch_scc0 .LBB0_926
	v_lshlrev_b32_e32 v74, 2, v73
	v_lshrrev_b32_e32 v75, 1, v73
	v_and_b32_e32 v74, 16, v74
	v_and_b32_e32 v75, 12, v75
	v_and_b32_e32 v76, 0xffffffe3, v73
	v_or3_b32 v74, v74, v76, v75
	s_mov_b64 s[28:29], 0

.LBB0_1071:
	v_mad_i64_i32 v[74:75], s[10:11], v74, s10, 0
	v_lshl_add_u64 v[74:75], v[74:75], 1, s[78:79]
	v_lshl_add_u64 v[74:75], s[74:75], 1, v[74:75]
	v_lshl_add_u64 v[74:75], v[74:75], 0, v[70:71]
	s_waitcnt lgkmcnt(0)
	global_store_dwordx4 v[74:75], v[66:69], off sc1 nt

.LBB0_1137:
	v_mov_b64_e32 v[76:77], s[78:79]
	v_mad_i64_i32 v[74:75], s[24:25], v74, s10, v[76:77]
	s_ashr_i32 s75, s74, 31
	v_lshl_add_u64 v[74:75], v[74:75], 0, s[74:75]
	v_lshl_add_u64 v[74:75], v[74:75], 0, v[178:179]
	s_waitcnt lgkmcnt(0)
	global_store_dwordx4 v[74:75], v[66:69], off sc1 nt
	ds_read_b128 v[66:69], v70 offset:16896
	s_cmp_lt_i32 s12, 1
	v_add_u32_e32 v73, s13, v194
	s_cbranch_scc1 .LBB0_1141
	s_cmp_eq_u32 s12, 1
	s_mov_b64 s[28:29], -1
	s_cbranch_scc0 .LBB0_1140
	v_lshlrev_b32_e32 v74, 2, v73
	v_lshrrev_b32_e32 v75, 1, v73
	v_and_b32_e32 v74, 16, v74
	v_and_b32_e32 v75, 12, v75
	v_and_b32_e32 v76, 0xffffffe3, v73
	v_or3_b32 v74, v74, v76, v75
	s_mov_b64 s[28:29], 0

.LBB0_1145:
	v_mov_b64_e32 v[76:77], s[78:79]
	v_mad_i64_i32 v[74:75], s[24:25], v74, s10, v[76:77]
	v_lshl_add_u64 v[74:75], v[74:75], 0, s[74:75]
	v_lshl_add_u64 v[74:75], v[74:75], 0, v[178:179]
	s_waitcnt lgkmcnt(0)
	global_store_dwordx4 v[74:75], v[66:69], off sc1 nt
	ds_read_b128 v[66:69], v70 offset:33792
	s_cmp_lt_i32 s12, 1
	v_add_u32_e32 v73, s13, v202
	s_cbranch_scc1 .LBB0_1149
	s_cmp_eq_u32 s12, 1
	s_mov_b64 s[28:29], -1
	s_cbranch_scc0 .LBB0_1148
	v_lshlrev_b32_e32 v74, 2, v73
	v_lshrrev_b32_e32 v75, 1, v73
	v_and_b32_e32 v74, 16, v74
	v_and_b32_e32 v75, 12, v75
	v_and_b32_e32 v76, 0xffffffe3, v73
	v_or3_b32 v74, v74, v76, v75
	s_mov_b64 s[28:29], 0

.LBB0_1153:
	v_mov_b64_e32 v[76:77], s[78:79]
	v_mad_i64_i32 v[74:75], s[24:25], v74, s10, v[76:77]
	v_lshl_add_u64 v[74:75], v[74:75], 0, s[74:75]
	v_lshl_add_u64 v[74:75], v[74:75], 0, v[178:179]
	s_waitcnt lgkmcnt(0)
	global_store_dwordx4 v[74:75], v[66:69], off sc1 nt
	ds_read_b128 v[66:69], v70 offset:50688
	s_cmp_lt_i32 s12, 1
	v_add_u32_e32 v70, s13, v203
	s_cbranch_scc1 .LBB0_1157
	s_cmp_eq_u32 s12, 1
	s_mov_b64 s[28:29], -1
	s_cbranch_scc0 .LBB0_1156
	v_lshlrev_b32_e32 v73, 2, v70
	v_lshrrev_b32_e32 v74, 1, v70
	v_and_b32_e32 v73, 16, v73
	v_and_b32_e32 v74, 12, v74
	v_and_b32_e32 v75, 0xffffffe3, v70
	v_or3_b32 v73, v73, v75, v74
	s_mov_b64 s[28:29], 0

.LBB0_1161:
	v_mov_b64_e32 v[74:75], s[78:79]
	v_mad_i64_i32 v[74:75], s[24:25], v73, s10, v[74:75]
	v_lshl_add_u64 v[74:75], v[74:75], 0, s[74:75]
	v_lshl_add_u64 v[74:75], v[74:75], 0, v[178:179]
	s_waitcnt lgkmcnt(0)
	global_store_dwordx4 v[74:75], v[66:69], off sc1 nt
	s_branch .LBB0_1072

.LBB0_1170:
	v_mad_i64_i32 v[74:75], s[24:25], v74, s10, 0
	v_lshl_add_u64 v[74:75], v[74:75], 1, s[78:79]
	s_ashr_i32 s75, s74, 31
	v_lshl_add_u64 v[74:75], s[74:75], 1, v[74:75]
	v_lshlrev_b32_e32 v70, 1, v195
	v_lshl_add_u64 v[74:75], v[74:75], 0, v[70:71]
	s_waitcnt lgkmcnt(0)
	global_store_dwordx4 v[74:75], v[66:69], off sc1 nt
	ds_read_b128 v[66:69], v73 offset:8448
	s_cmp_lt_i32 s12, 1
	v_add_u32_e32 v74, s13, v207
	s_cbranch_scc1 .LBB0_1174
	s_cmp_eq_u32 s12, 1
	s_mov_b64 s[28:29], -1
	s_cbranch_scc0 .LBB0_1173
	v_lshlrev_b32_e32 v75, 2, v74
	v_lshrrev_b32_e32 v76, 1, v74
	v_and_b32_e32 v75, 16, v75
	v_and_b32_e32 v76, 12, v76
	v_and_b32_e32 v77, 0xffffffe3, v74
	v_or3_b32 v75, v75, v77, v76
	s_mov_b64 s[28:29], 0

.LBB0_1178:
	v_mad_i64_i32 v[74:75], s[24:25], v75, s10, 0
	v_lshl_add_u64 v[74:75], v[74:75], 1, s[78:79]
	v_lshl_add_u64 v[74:75], s[74:75], 1, v[74:75]
	v_lshl_add_u64 v[74:75], v[74:75], 0, v[70:71]
	s_waitcnt lgkmcnt(0)
	global_store_dwordx4 v[74:75], v[66:69], off sc1 nt
	ds_read_b128 v[66:69], v73 offset:16896
	s_cmp_lt_i32 s12, 1
	v_add_u32_e32 v74, s13, v213
	s_cbranch_scc1 .LBB0_1182
	s_cmp_eq_u32 s12, 1
	s_mov_b64 s[28:29], -1
	s_cbranch_scc0 .LBB0_1181
	v_lshlrev_b32_e32 v75, 2, v74
	v_lshrrev_b32_e32 v76, 1, v74
	v_and_b32_e32 v75, 16, v75
	v_and_b32_e32 v76, 12, v76
	v_and_b32_e32 v77, 0xffffffe3, v74
	v_or3_b32 v75, v75, v77, v76
	s_mov_b64 s[28:29], 0

.LBB0_1186:
	v_mad_i64_i32 v[74:75], s[24:25], v75, s10, 0
	v_lshl_add_u64 v[74:75], v[74:75], 1, s[78:79]
	v_lshl_add_u64 v[74:75], s[74:75], 1, v[74:75]
	v_lshl_add_u64 v[74:75], v[74:75], 0, v[70:71]
	s_waitcnt lgkmcnt(0)
	global_store_dwordx4 v[74:75], v[66:69], off sc1 nt
	ds_read_b128 v[66:69], v73 offset:25344
	s_cmp_lt_i32 s12, 1
	v_add_u32_e32 v74, s13, v208
	s_cbranch_scc1 .LBB0_1190
	s_cmp_eq_u32 s12, 1
	s_mov_b64 s[28:29], -1
	s_cbranch_scc0 .LBB0_1189
	v_lshlrev_b32_e32 v75, 2, v74
	v_lshrrev_b32_e32 v76, 1, v74
	v_and_b32_e32 v75, 16, v75
	v_and_b32_e32 v76, 12, v76
	v_and_b32_e32 v77, 0xffffffe3, v74
	v_or3_b32 v75, v75, v77, v76
	s_mov_b64 s[28:29], 0

.LBB0_1194:
	v_mad_i64_i32 v[74:75], s[24:25], v75, s10, 0
	v_lshl_add_u64 v[74:75], v[74:75], 1, s[78:79]
	v_lshl_add_u64 v[74:75], s[74:75], 1, v[74:75]
	v_lshl_add_u64 v[74:75], v[74:75], 0, v[70:71]
	s_waitcnt lgkmcnt(0)
	global_store_dwordx4 v[74:75], v[66:69], off sc1 nt
	ds_read_b128 v[66:69], v73 offset:33792
	s_cmp_lt_i32 s12, 1
	v_add_u32_e32 v74, s13, v209
	s_cbranch_scc1 .LBB0_1198
	s_cmp_eq_u32 s12, 1
	s_mov_b64 s[28:29], -1
	s_cbranch_scc0 .LBB0_1197
	v_lshlrev_b32_e32 v75, 2, v74
	v_lshrrev_b32_e32 v76, 1, v74
	v_and_b32_e32 v75, 16, v75
	v_and_b32_e32 v76, 12, v76
	v_and_b32_e32 v77, 0xffffffe3, v74
	v_or3_b32 v75, v75, v77, v76
	s_mov_b64 s[28:29], 0

.LBB0_1202:
	v_mad_i64_i32 v[74:75], s[24:25], v75, s10, 0
	v_lshl_add_u64 v[74:75], v[74:75], 1, s[78:79]
	v_lshl_add_u64 v[74:75], s[74:75], 1, v[74:75]
	v_lshl_add_u64 v[74:75], v[74:75], 0, v[70:71]
	s_waitcnt lgkmcnt(0)
	global_store_dwordx4 v[74:75], v[66:69], off sc1 nt
	ds_read_b128 v[66:69], v73 offset:42240
	s_cmp_lt_i32 s12, 1
	v_add_u32_e32 v74, s13, v210
	s_cbranch_scc1 .LBB0_1206
	s_cmp_eq_u32 s12, 1
	s_mov_b64 s[28:29], -1
	s_cbranch_scc0 .LBB0_1205
	v_lshlrev_b32_e32 v75, 2, v74
	v_lshrrev_b32_e32 v76, 1, v74
	v_and_b32_e32 v75, 16, v75
	v_and_b32_e32 v76, 12, v76
	v_and_b32_e32 v77, 0xffffffe3, v74
	v_or3_b32 v75, v75, v77, v76
	s_mov_b64 s[28:29], 0

.LBB0_1210:
	v_mad_i64_i32 v[74:75], s[24:25], v75, s10, 0
	v_lshl_add_u64 v[74:75], v[74:75], 1, s[78:79]
	v_lshl_add_u64 v[74:75], s[74:75], 1, v[74:75]
	v_lshl_add_u64 v[74:75], v[74:75], 0, v[70:71]
	s_waitcnt lgkmcnt(0)
	global_store_dwordx4 v[74:75], v[66:69], off sc1 nt
	ds_read_b128 v[66:69], v73 offset:50688
	s_cmp_lt_i32 s12, 1
	v_add_u32_e32 v74, s13, v211
	s_cbranch_scc1 .LBB0_1214
	s_cmp_eq_u32 s12, 1
	s_mov_b64 s[28:29], -1
	s_cbranch_scc0 .LBB0_1213
	v_lshlrev_b32_e32 v75, 2, v74
	v_lshrrev_b32_e32 v76, 1, v74
	v_and_b32_e32 v75, 16, v75
	v_and_b32_e32 v76, 12, v76
	v_and_b32_e32 v77, 0xffffffe3, v74
	v_or3_b32 v75, v75, v77, v76
	s_mov_b64 s[28:29], 0

.LBB0_1218:
	v_mad_i64_i32 v[74:75], s[24:25], v75, s10, 0
	v_lshl_add_u64 v[74:75], v[74:75], 1, s[78:79]
	v_lshl_add_u64 v[74:75], s[74:75], 1, v[74:75]
	v_lshl_add_u64 v[74:75], v[74:75], 0, v[70:71]
	s_waitcnt lgkmcnt(0)
	global_store_dwordx4 v[74:75], v[66:69], off sc1 nt
	ds_read_b128 v[66:69], v73 offset:59136
	s_cmp_lt_i32 s12, 1
	v_add_u32_e32 v73, s13, v212
	s_cbranch_scc1 .LBB0_1222
	s_cmp_eq_u32 s12, 1
	s_mov_b64 s[28:29], -1
	s_cbranch_scc0 .LBB0_1221
	v_lshlrev_b32_e32 v74, 2, v73
	v_lshrrev_b32_e32 v75, 1, v73
	v_and_b32_e32 v74, 16, v74
	v_and_b32_e32 v75, 12, v75
	v_and_b32_e32 v76, 0xffffffe3, v73
	v_or3_b32 v74, v74, v76, v75
	s_mov_b64 s[28:29], 0

.LBB0_1552:
	v_mad_i64_i32 v[90:91], s[26:27], v89, s26, 0
	v_lshl_add_u64 v[90:91], v[90:91], 1, s[84:85]
	v_lshl_add_u64 v[90:91], s[82:83], 1, v[90:91]
	v_mov_b32_e32 v77, v71
	v_lshl_add_u64 v[76:77], v[90:91], 0, v[76:77]
	s_waitcnt lgkmcnt(0)
	global_store_dwordx4 v[76:77], v[66:69], off sc1 nt

.LBB0_1607:
	v_mov_b64_e32 v[90:91], s[84:85]
	v_mad_i64_i32 v[90:91], s[28:29], v77, s26, v[90:91]
	s_ashr_i32 s83, s82, 31
	v_lshl_add_u64 v[90:91], v[90:91], 0, s[82:83]
	v_lshl_add_u64 v[90:91], v[90:91], 0, v[72:73]
	s_waitcnt lgkmcnt(0)
	global_store_dwordx4 v[90:91], v[66:69], off sc1 nt
	ds_read_b128 v[66:69], v87 offset:16896
	s_cmp_lt_i32 s33, 1
	v_add_u32_e32 v77, 32, v76
	s_cbranch_scc1 .LBB0_1611
	s_cmp_eq_u32 s33, 1
	s_mov_b64 s[28:29], -1
	s_cbranch_scc0 .LBB0_1610
	v_lshlrev_b32_e32 v89, 2, v77
	v_lshrrev_b32_e32 v90, 1, v77
	v_and_b32_e32 v89, 16, v89
	v_and_b32_e32 v90, 12, v90
	v_and_b32_e32 v91, 0xffffffe3, v77
	v_or3_b32 v89, v89, v91, v90
	s_mov_b64 s[28:29], 0

.LBB0_1615:
	v_mov_b64_e32 v[90:91], s[84:85]
	v_mad_i64_i32 v[90:91], s[28:29], v89, s26, v[90:91]
	v_lshl_add_u64 v[90:91], v[90:91], 0, s[82:83]
	v_lshl_add_u64 v[90:91], v[90:91], 0, v[72:73]
	s_waitcnt lgkmcnt(0)
	global_store_dwordx4 v[90:91], v[66:69], off sc1 nt
	ds_read_b128 v[66:69], v87 offset:33792
	s_cmp_lt_i32 s33, 1
	v_add_u32_e32 v77, s52, v1
	s_cbranch_scc1 .LBB0_1619
	s_cmp_eq_u32 s33, 1
	s_mov_b64 s[28:29], -1
	s_cbranch_scc0 .LBB0_1618
	v_lshlrev_b32_e32 v89, 2, v77
	v_lshrrev_b32_e32 v90, 1, v77
	v_and_b32_e32 v89, 16, v89
	v_and_b32_e32 v90, 12, v90
	v_and_b32_e32 v91, 0xffffffe3, v77
	v_or3_b32 v89, v89, v91, v90
	s_mov_b64 s[28:29], 0

.LBB0_1623:
	v_mov_b64_e32 v[90:91], s[84:85]
	v_mad_i64_i32 v[90:91], s[28:29], v89, s26, v[90:91]
	v_lshl_add_u64 v[90:91], v[90:91], 0, s[82:83]
	v_lshl_add_u64 v[90:91], v[90:91], 0, v[72:73]
	s_waitcnt lgkmcnt(0)
	global_store_dwordx4 v[90:91], v[66:69], off sc1 nt
	ds_read_b128 v[66:69], v87 offset:50688
	s_cmp_lt_i32 s33, 1
	v_add_u32_e32 v76, 0x60, v76
	s_cbranch_scc1 .LBB0_1627
	s_cmp_eq_u32 s33, 1
	s_mov_b64 s[28:29], -1
	s_cbranch_scc0 .LBB0_1626
	v_lshlrev_b32_e32 v77, 2, v76
	v_lshrrev_b32_e32 v89, 1, v76
	v_and_b32_e32 v77, 16, v77
	v_and_b32_e32 v89, 12, v89
	v_and_b32_e32 v90, 0xffffffe3, v76
	v_or3_b32 v77, v77, v90, v89
	s_mov_b64 s[28:29], 0

.LBB0_1631:
	v_mov_b64_e32 v[90:91], s[84:85]
	v_mad_i64_i32 v[76:77], s[28:29], v77, s26, v[90:91]
	v_lshl_add_u64 v[76:77], v[76:77], 0, s[82:83]
	v_lshl_add_u64 v[76:77], v[76:77], 0, v[72:73]
	s_waitcnt lgkmcnt(0)
	global_store_dwordx4 v[76:77], v[66:69], off sc1 nt
	s_branch .LBB0_1553

.LBB0_1640:
	v_mad_i64_i32 v[76:77], s[28:29], v76, s26, 0
	v_lshl_add_u64 v[76:77], v[76:77], 1, s[84:85]
	s_ashr_i32 s83, s82, 31
	v_lshl_add_u64 v[90:91], s[82:83], 1, v[76:77]
	v_lshlrev_b32_e32 v76, 1, v74
	v_mov_b32_e32 v77, v71
	v_lshl_add_u64 v[90:91], v[90:91], 0, v[76:77]
	s_waitcnt lgkmcnt(0)
	global_store_dwordx4 v[90:91], v[66:69], off sc1 nt
	ds_read_b128 v[66:69], v88 offset:8448
	s_cmp_lt_i32 s33, 1
	v_add_u32_e32 v77, 16, v89
	s_cbranch_scc1 .LBB0_1644
	s_cmp_eq_u32 s33, 1
	s_mov_b64 s[28:29], -1
	s_cbranch_scc0 .LBB0_1643
	v_lshlrev_b32_e32 v90, 2, v77
	v_lshrrev_b32_e32 v91, 1, v77
	v_and_b32_e32 v90, 16, v90
	v_and_b32_e32 v91, 12, v91
	v_and_b32_e32 v92, 0xffffffe3, v77
	v_or3_b32 v90, v90, v92, v91
	s_mov_b64 s[28:29], 0

.LBB0_1648:
	v_mad_i64_i32 v[90:91], s[28:29], v90, s26, 0
	v_lshl_add_u64 v[90:91], v[90:91], 1, s[84:85]
	v_lshl_add_u64 v[90:91], s[82:83], 1, v[90:91]
	v_mov_b32_e32 v77, v71
	v_lshl_add_u64 v[90:91], v[90:91], 0, v[76:77]
	s_waitcnt lgkmcnt(0)
	global_store_dwordx4 v[90:91], v[66:69], off sc1 nt
	ds_read_b128 v[66:69], v88 offset:16896
	s_cmp_lt_i32 s33, 1
	v_add_u32_e32 v77, s52, v82
	s_cbranch_scc1 .LBB0_1652
	s_cmp_eq_u32 s33, 1
	s_mov_b64 s[28:29], -1
	s_cbranch_scc0 .LBB0_1651
	v_lshlrev_b32_e32 v90, 2, v77
	v_lshrrev_b32_e32 v91, 1, v77
	v_and_b32_e32 v90, 16, v90
	v_and_b32_e32 v91, 12, v91
	v_and_b32_e32 v92, 0xffffffe3, v77
	v_or3_b32 v90, v90, v92, v91
	s_mov_b64 s[28:29], 0

.LBB0_1656:
	v_mad_i64_i32 v[90:91], s[28:29], v90, s26, 0
	v_lshl_add_u64 v[90:91], v[90:91], 1, s[84:85]
	v_lshl_add_u64 v[90:91], s[82:83], 1, v[90:91]
	v_mov_b32_e32 v77, v71
	v_lshl_add_u64 v[90:91], v[90:91], 0, v[76:77]
	s_waitcnt lgkmcnt(0)
	global_store_dwordx4 v[90:91], v[66:69], off sc1 nt
	ds_read_b128 v[66:69], v88 offset:25344
	s_cmp_lt_i32 s33, 1
	v_add_u32_e32 v77, 48, v89
	s_cbranch_scc1 .LBB0_1660
	s_cmp_eq_u32 s33, 1
	s_mov_b64 s[28:29], -1
	s_cbranch_scc0 .LBB0_1659
	v_lshlrev_b32_e32 v90, 2, v77
	v_lshrrev_b32_e32 v91, 1, v77
	v_and_b32_e32 v90, 16, v90
	v_and_b32_e32 v91, 12, v91
	v_and_b32_e32 v92, 0xffffffe3, v77
	v_or3_b32 v90, v90, v92, v91
	s_mov_b64 s[28:29], 0

.LBB0_1664:
	v_mad_i64_i32 v[90:91], s[28:29], v90, s26, 0
	v_lshl_add_u64 v[90:91], v[90:91], 1, s[84:85]
	v_lshl_add_u64 v[90:91], s[82:83], 1, v[90:91]
	v_mov_b32_e32 v77, v71
	v_lshl_add_u64 v[90:91], v[90:91], 0, v[76:77]
	s_waitcnt lgkmcnt(0)
	global_store_dwordx4 v[90:91], v[66:69], off sc1 nt
	ds_read_b128 v[66:69], v88 offset:33792
	s_cmp_lt_i32 s33, 1
	v_add_u32_e32 v77, s52, v83
	s_cbranch_scc1 .LBB0_1668
	s_cmp_eq_u32 s33, 1
	s_mov_b64 s[28:29], -1
	s_cbranch_scc0 .LBB0_1667
	v_lshlrev_b32_e32 v90, 2, v77
	v_lshrrev_b32_e32 v91, 1, v77
	v_and_b32_e32 v90, 16, v90
	v_and_b32_e32 v91, 12, v91
	v_and_b32_e32 v92, 0xffffffe3, v77
	v_or3_b32 v90, v90, v92, v91
	s_mov_b64 s[28:29], 0

.LBB0_1672:
	v_mad_i64_i32 v[90:91], s[28:29], v90, s26, 0
	v_lshl_add_u64 v[90:91], v[90:91], 1, s[84:85]
	v_lshl_add_u64 v[90:91], s[82:83], 1, v[90:91]
	v_mov_b32_e32 v77, v71
	v_lshl_add_u64 v[90:91], v[90:91], 0, v[76:77]
	s_waitcnt lgkmcnt(0)
	global_store_dwordx4 v[90:91], v[66:69], off sc1 nt
	ds_read_b128 v[66:69], v88 offset:42240
	s_cmp_lt_i32 s33, 1
	v_add_u32_e32 v77, 0x50, v89
	s_cbranch_scc1 .LBB0_1676
	s_cmp_eq_u32 s33, 1
	s_mov_b64 s[28:29], -1
	s_cbranch_scc0 .LBB0_1675
	v_lshlrev_b32_e32 v90, 2, v77
	v_lshrrev_b32_e32 v91, 1, v77
	v_and_b32_e32 v90, 16, v90
	v_and_b32_e32 v91, 12, v91
	v_and_b32_e32 v92, 0xffffffe3, v77
	v_or3_b32 v90, v90, v92, v91
	s_mov_b64 s[28:29], 0

.LBB0_1680:
	v_mad_i64_i32 v[90:91], s[28:29], v90, s26, 0
	v_lshl_add_u64 v[90:91], v[90:91], 1, s[84:85]
	v_lshl_add_u64 v[90:91], s[82:83], 1, v[90:91]
	v_mov_b32_e32 v77, v71
	v_lshl_add_u64 v[90:91], v[90:91], 0, v[76:77]
	s_waitcnt lgkmcnt(0)
	global_store_dwordx4 v[90:91], v[66:69], off sc1 nt
	ds_read_b128 v[66:69], v88 offset:50688
	s_cmp_lt_i32 s33, 1
	v_add_u32_e32 v77, s52, v84
	s_cbranch_scc1 .LBB0_1684
	s_cmp_eq_u32 s33, 1
	s_mov_b64 s[28:29], -1
	s_cbranch_scc0 .LBB0_1683
	v_lshlrev_b32_e32 v90, 2, v77
	v_lshrrev_b32_e32 v91, 1, v77
	v_and_b32_e32 v90, 16, v90
	v_and_b32_e32 v91, 12, v91
	v_and_b32_e32 v92, 0xffffffe3, v77
	v_or3_b32 v90, v90, v92, v91
	s_mov_b64 s[28:29], 0

.LBB0_1688:
	v_mad_i64_i32 v[90:91], s[28:29], v90, s26, 0
	v_lshl_add_u64 v[90:91], v[90:91], 1, s[84:85]
	v_lshl_add_u64 v[90:91], s[82:83], 1, v[90:91]
	v_mov_b32_e32 v77, v71
	v_lshl_add_u64 v[90:91], v[90:91], 0, v[76:77]
	s_waitcnt lgkmcnt(0)
	global_store_dwordx4 v[90:91], v[66:69], off sc1 nt
	ds_read_b128 v[66:69], v88 offset:59136
	s_cmp_lt_i32 s33, 1
	v_add_u32_e32 v77, 0x70, v89
	s_cbranch_scc1 .LBB0_1692
	s_cmp_eq_u32 s33, 1
	s_mov_b64 s[28:29], -1
	s_cbranch_scc0 .LBB0_1691
	v_lshlrev_b32_e32 v89, 2, v77
	v_lshrrev_b32_e32 v90, 1, v77
	v_and_b32_e32 v89, 16, v89
	v_and_b32_e32 v90, 12, v90
	v_and_b32_e32 v91, 0xffffffe3, v77
	v_or3_b32 v89, v89, v91, v90
	s_mov_b64 s[28:29], 0

.LBB0_2104:
	v_mad_i64_i32 v[84:85], s[10:11], v79, s10, 0
	v_lshl_add_u64 v[84:85], v[84:85], 1, s[76:77]
	v_lshl_add_u64 v[84:85], s[68:69], 1, v[84:85]
	v_lshl_add_u64 v[84:85], v[84:85], 0, v[74:75]
	s_waitcnt lgkmcnt(0)
	global_store_dwordx4 v[84:85], v[66:69], off sc1 nt

.LBB0_2169:
	v_mov_b64_e32 v[84:85], s[76:77]
	v_mad_i64_i32 v[84:85], s[28:29], v79, s10, v[84:85]
	s_ashr_i32 s69, s68, 31
	v_lshl_add_u64 v[84:85], v[84:85], 0, s[68:69]
	v_lshl_add_u64 v[84:85], v[84:85], 0, v[178:179]
	s_waitcnt lgkmcnt(0)
	global_store_dwordx4 v[84:85], v[66:69], off sc1 nt
	ds_read_b128 v[66:69], v74 offset:16896
	s_cmp_lt_i32 s18, 1
	v_add_u32_e32 v77, s19, v194
	s_cbranch_scc1 .LBB0_2173
	s_cmp_eq_u32 s18, 1
	s_mov_b64 s[28:29], -1
	s_cbranch_scc0 .LBB0_2172
	v_lshlrev_b32_e32 v79, 2, v77
	v_lshrrev_b32_e32 v83, 1, v77
	v_and_b32_e32 v79, 16, v79
	v_and_b32_e32 v83, 12, v83
	v_and_b32_e32 v84, 0xffffffe3, v77
	v_or3_b32 v79, v79, v84, v83
	s_mov_b64 s[28:29], 0

.LBB0_2177:
	v_mov_b64_e32 v[84:85], s[76:77]
	v_mad_i64_i32 v[84:85], s[28:29], v79, s10, v[84:85]
	v_lshl_add_u64 v[84:85], v[84:85], 0, s[68:69]
	v_lshl_add_u64 v[84:85], v[84:85], 0, v[178:179]
	s_waitcnt lgkmcnt(0)
	global_store_dwordx4 v[84:85], v[66:69], off sc1 nt
	ds_read_b128 v[66:69], v74 offset:33792
	s_cmp_lt_i32 s18, 1
	v_add_u32_e32 v77, s19, v202
	s_cbranch_scc1 .LBB0_2181
	s_cmp_eq_u32 s18, 1
	s_mov_b64 s[28:29], -1
	s_cbranch_scc0 .LBB0_2180
	v_lshlrev_b32_e32 v79, 2, v77
	v_lshrrev_b32_e32 v83, 1, v77
	v_and_b32_e32 v79, 16, v79
	v_and_b32_e32 v83, 12, v83
	v_and_b32_e32 v84, 0xffffffe3, v77
	v_or3_b32 v79, v79, v84, v83
	s_mov_b64 s[28:29], 0

.LBB0_2185:
	v_mov_b64_e32 v[84:85], s[76:77]
	v_mad_i64_i32 v[84:85], s[28:29], v79, s10, v[84:85]
	v_lshl_add_u64 v[84:85], v[84:85], 0, s[68:69]
	v_lshl_add_u64 v[84:85], v[84:85], 0, v[178:179]
	s_waitcnt lgkmcnt(0)
	global_store_dwordx4 v[84:85], v[66:69], off sc1 nt
	ds_read_b128 v[66:69], v74 offset:50688
	s_cmp_lt_i32 s18, 1
	v_add_u32_e32 v74, s19, v203
	s_cbranch_scc1 .LBB0_2189
	s_cmp_eq_u32 s18, 1
	s_mov_b64 s[28:29], -1
	s_cbranch_scc0 .LBB0_2188
	v_lshlrev_b32_e32 v77, 2, v74
	v_lshrrev_b32_e32 v79, 1, v74
	v_and_b32_e32 v77, 16, v77
	v_and_b32_e32 v79, 12, v79
	v_and_b32_e32 v83, 0xffffffe3, v74
	v_or3_b32 v77, v77, v83, v79
	s_mov_b64 s[28:29], 0

.LBB0_2193:
	v_mov_b64_e32 v[84:85], s[76:77]
	v_mad_i64_i32 v[84:85], s[28:29], v77, s10, v[84:85]
	v_lshl_add_u64 v[84:85], v[84:85], 0, s[68:69]
	v_lshl_add_u64 v[84:85], v[84:85], 0, v[178:179]
	s_waitcnt lgkmcnt(0)
	global_store_dwordx4 v[84:85], v[66:69], off sc1 nt
	s_branch .LBB0_2105

.LBB0_2202:
	v_mad_i64_i32 v[84:85], s[28:29], v79, s10, 0
	v_lshl_add_u64 v[84:85], v[84:85], 1, s[76:77]
	s_ashr_i32 s69, s68, 31
	v_lshl_add_u64 v[84:85], s[68:69], 1, v[84:85]
	v_lshlrev_b32_e32 v74, 1, v195
	v_lshl_add_u64 v[84:85], v[84:85], 0, v[74:75]
	s_waitcnt lgkmcnt(0)
	global_store_dwordx4 v[84:85], v[66:69], off sc1 nt
	ds_read_b128 v[66:69], v77 offset:8448
	s_cmp_lt_i32 s18, 1
	v_add_u32_e32 v79, s19, v213
	s_cbranch_scc1 .LBB0_2206
	s_cmp_eq_u32 s18, 1
	s_mov_b64 s[28:29], -1
	s_cbranch_scc0 .LBB0_2205
	v_lshlrev_b32_e32 v83, 2, v79
	v_lshrrev_b32_e32 v84, 1, v79
	v_and_b32_e32 v83, 16, v83
	v_and_b32_e32 v84, 12, v84
	v_and_b32_e32 v85, 0xffffffe3, v79
	v_or3_b32 v83, v83, v85, v84
	s_mov_b64 s[28:29], 0

.LBB0_2210:
	v_mad_i64_i32 v[84:85], s[28:29], v83, s10, 0
	v_lshl_add_u64 v[84:85], v[84:85], 1, s[76:77]
	v_lshl_add_u64 v[84:85], s[68:69], 1, v[84:85]
	v_lshl_add_u64 v[84:85], v[84:85], 0, v[74:75]
	s_waitcnt lgkmcnt(0)
	global_store_dwordx4 v[84:85], v[66:69], off sc1 nt
	ds_read_b128 v[66:69], v77 offset:16896
	s_cmp_lt_i32 s18, 1
	v_add_u32_e32 v79, s19, v209
	s_cbranch_scc1 .LBB0_2214
	s_cmp_eq_u32 s18, 1
	s_mov_b64 s[28:29], -1
	s_cbranch_scc0 .LBB0_2213
	v_lshlrev_b32_e32 v83, 2, v79
	v_lshrrev_b32_e32 v84, 1, v79
	v_and_b32_e32 v83, 16, v83
	v_and_b32_e32 v84, 12, v84
	v_and_b32_e32 v85, 0xffffffe3, v79
	v_or3_b32 v83, v83, v85, v84
	s_mov_b64 s[28:29], 0

.LBB0_2218:
	v_mad_i64_i32 v[84:85], s[28:29], v83, s10, 0
	v_lshl_add_u64 v[84:85], v[84:85], 1, s[76:77]
	v_lshl_add_u64 v[84:85], s[68:69], 1, v[84:85]
	v_lshl_add_u64 v[84:85], v[84:85], 0, v[74:75]
	s_waitcnt lgkmcnt(0)
	global_store_dwordx4 v[84:85], v[66:69], off sc1 nt
	ds_read_b128 v[66:69], v77 offset:25344
	s_cmp_lt_i32 s18, 1
	v_add_u32_e32 v79, s19, v208
	s_cbranch_scc1 .LBB0_2222
	s_cmp_eq_u32 s18, 1
	s_mov_b64 s[28:29], -1
	s_cbranch_scc0 .LBB0_2221
	v_lshlrev_b32_e32 v83, 2, v79
	v_lshrrev_b32_e32 v84, 1, v79
	v_and_b32_e32 v83, 16, v83
	v_and_b32_e32 v84, 12, v84
	v_and_b32_e32 v85, 0xffffffe3, v79
	v_or3_b32 v83, v83, v85, v84
	s_mov_b64 s[28:29], 0

.LBB0_2226:
	v_mad_i64_i32 v[84:85], s[28:29], v83, s10, 0
	v_lshl_add_u64 v[84:85], v[84:85], 1, s[76:77]
	v_lshl_add_u64 v[84:85], s[68:69], 1, v[84:85]
	v_lshl_add_u64 v[84:85], v[84:85], 0, v[74:75]
	s_waitcnt lgkmcnt(0)
	global_store_dwordx4 v[84:85], v[66:69], off sc1 nt
	ds_read_b128 v[66:69], v77 offset:33792
	s_cmp_lt_i32 s18, 1
	v_add_u32_e32 v79, s19, v211
	s_cbranch_scc1 .LBB0_2230
	s_cmp_eq_u32 s18, 1
	s_mov_b64 s[28:29], -1
	s_cbranch_scc0 .LBB0_2229
	v_lshlrev_b32_e32 v83, 2, v79
	v_lshrrev_b32_e32 v84, 1, v79
	v_and_b32_e32 v83, 16, v83
	v_and_b32_e32 v84, 12, v84
	v_and_b32_e32 v85, 0xffffffe3, v79
	v_or3_b32 v83, v83, v85, v84
	s_mov_b64 s[28:29], 0

.LBB0_2234:
	v_mad_i64_i32 v[84:85], s[28:29], v83, s10, 0
	v_lshl_add_u64 v[84:85], v[84:85], 1, s[76:77]
	v_lshl_add_u64 v[84:85], s[68:69], 1, v[84:85]
	v_lshl_add_u64 v[84:85], v[84:85], 0, v[74:75]
	s_waitcnt lgkmcnt(0)
	global_store_dwordx4 v[84:85], v[66:69], off sc1 nt
	ds_read_b128 v[66:69], v77 offset:42240
	s_cmp_lt_i32 s18, 1
	v_add_u32_e32 v79, s19, v210
	s_cbranch_scc1 .LBB0_2238
	s_cmp_eq_u32 s18, 1
	s_mov_b64 s[28:29], -1
	s_cbranch_scc0 .LBB0_2237
	v_lshlrev_b32_e32 v83, 2, v79
	v_lshrrev_b32_e32 v84, 1, v79
	v_and_b32_e32 v83, 16, v83
	v_and_b32_e32 v84, 12, v84
	v_and_b32_e32 v85, 0xffffffe3, v79
	v_or3_b32 v83, v83, v85, v84
	s_mov_b64 s[28:29], 0

.LBB0_2242:
	v_mad_i64_i32 v[84:85], s[28:29], v83, s10, 0
	v_lshl_add_u64 v[84:85], v[84:85], 1, s[76:77]
	v_lshl_add_u64 v[84:85], s[68:69], 1, v[84:85]
	v_lshl_add_u64 v[84:85], v[84:85], 0, v[74:75]
	s_waitcnt lgkmcnt(0)
	global_store_dwordx4 v[84:85], v[66:69], off sc1 nt
	ds_read_b128 v[66:69], v77 offset:50688
	s_cmp_lt_i32 s18, 1
	v_add_u32_e32 v79, s19, v97
	s_cbranch_scc1 .LBB0_2246
	s_cmp_eq_u32 s18, 1
	s_mov_b64 s[28:29], -1
	s_cbranch_scc0 .LBB0_2245
	v_lshlrev_b32_e32 v83, 2, v79
	v_lshrrev_b32_e32 v84, 1, v79
	v_and_b32_e32 v83, 16, v83
	v_and_b32_e32 v84, 12, v84
	v_and_b32_e32 v85, 0xffffffe3, v79
	v_or3_b32 v83, v83, v85, v84
	s_mov_b64 s[28:29], 0

.LBB0_2250:
	v_mad_i64_i32 v[84:85], s[28:29], v83, s10, 0
	v_lshl_add_u64 v[84:85], v[84:85], 1, s[76:77]
	v_lshl_add_u64 v[84:85], s[68:69], 1, v[84:85]
	v_lshl_add_u64 v[84:85], v[84:85], 0, v[74:75]
	s_waitcnt lgkmcnt(0)
	global_store_dwordx4 v[84:85], v[66:69], off sc1 nt
	ds_read_b128 v[66:69], v77 offset:59136
	s_cmp_lt_i32 s18, 1
	v_add_u32_e32 v77, s19, v212
	s_cbranch_scc1 .LBB0_2254
	s_cmp_eq_u32 s18, 1
	s_mov_b64 s[28:29], -1
	s_cbranch_scc0 .LBB0_2253
	v_lshlrev_b32_e32 v79, 2, v77
	v_lshrrev_b32_e32 v83, 1, v77
	v_and_b32_e32 v79, 16, v79
	v_and_b32_e32 v83, 12, v83
	v_and_b32_e32 v84, 0xffffffe3, v77
	v_or3_b32 v79, v79, v84, v83
	s_mov_b64 s[28:29], 0

.LBB0_2345:
	v_mad_i64_i32 v[74:75], s[10:11], v74, s10, 0
	v_lshl_add_u64 v[74:75], v[74:75], 1, s[26:27]
	v_lshl_add_u64 v[74:75], s[20:21], 1, v[74:75]
	v_lshl_add_u64 v[74:75], v[74:75], 0, v[70:71]
	s_waitcnt lgkmcnt(0)
	global_store_dwordx4 v[74:75], v[66:69], off sc1 nt

.LBB0_2410:
	v_mov_b64_e32 v[76:77], s[26:27]
	v_mad_i64_i32 v[74:75], s[28:29], v74, s10, v[76:77]
	s_ashr_i32 s21, s20, 31
	v_lshl_add_u64 v[74:75], v[74:75], 0, s[20:21]
	v_lshl_add_u64 v[74:75], v[74:75], 0, v[178:179]
	s_waitcnt lgkmcnt(0)
	global_store_dwordx4 v[74:75], v[66:69], off sc1 nt
	ds_read_b128 v[66:69], v70 offset:16896
	s_cmp_lt_i32 s22, 1
	v_add_u32_e32 v73, s23, v194
	s_cbranch_scc1 .LBB0_2414
	s_cmp_eq_u32 s22, 1
	s_mov_b64 s[28:29], -1
	s_cbranch_scc0 .LBB0_2413
	v_lshlrev_b32_e32 v74, 2, v73
	v_lshrrev_b32_e32 v75, 1, v73
	v_and_b32_e32 v74, 16, v74
	v_and_b32_e32 v75, 12, v75
	v_and_b32_e32 v76, 0xffffffe3, v73
	v_or3_b32 v74, v74, v76, v75
	s_mov_b64 s[28:29], 0

.LBB0_2418:
	v_mov_b64_e32 v[76:77], s[26:27]
	v_mad_i64_i32 v[74:75], s[28:29], v74, s10, v[76:77]
	v_lshl_add_u64 v[74:75], v[74:75], 0, s[20:21]
	v_lshl_add_u64 v[74:75], v[74:75], 0, v[178:179]
	s_waitcnt lgkmcnt(0)
	global_store_dwordx4 v[74:75], v[66:69], off sc1 nt
	ds_read_b128 v[66:69], v70 offset:33792
	s_cmp_lt_i32 s22, 1
	v_add_u32_e32 v73, s23, v202
	s_cbranch_scc1 .LBB0_2422
	s_cmp_eq_u32 s22, 1
	s_mov_b64 s[28:29], -1
	s_cbranch_scc0 .LBB0_2421
	v_lshlrev_b32_e32 v74, 2, v73
	v_lshrrev_b32_e32 v75, 1, v73
	v_and_b32_e32 v74, 16, v74
	v_and_b32_e32 v75, 12, v75
	v_and_b32_e32 v76, 0xffffffe3, v73
	v_or3_b32 v74, v74, v76, v75
	s_mov_b64 s[28:29], 0

.LBB0_2426:
	v_mov_b64_e32 v[76:77], s[26:27]
	v_mad_i64_i32 v[74:75], s[28:29], v74, s10, v[76:77]
	v_lshl_add_u64 v[74:75], v[74:75], 0, s[20:21]
	v_lshl_add_u64 v[74:75], v[74:75], 0, v[178:179]
	s_waitcnt lgkmcnt(0)
	global_store_dwordx4 v[74:75], v[66:69], off sc1 nt
	ds_read_b128 v[66:69], v70 offset:50688
	s_cmp_lt_i32 s22, 1
	v_add_u32_e32 v70, s23, v203
	s_cbranch_scc1 .LBB0_2430
	s_cmp_eq_u32 s22, 1
	s_mov_b64 s[28:29], -1
	s_cbranch_scc0 .LBB0_2429
	v_lshlrev_b32_e32 v73, 2, v70
	v_lshrrev_b32_e32 v74, 1, v70
	v_and_b32_e32 v73, 16, v73
	v_and_b32_e32 v74, 12, v74
	v_and_b32_e32 v75, 0xffffffe3, v70
	v_or3_b32 v73, v73, v75, v74
	s_mov_b64 s[28:29], 0

.LBB0_2434:
	v_mov_b64_e32 v[74:75], s[26:27]
	v_mad_i64_i32 v[74:75], s[28:29], v73, s10, v[74:75]
	v_lshl_add_u64 v[74:75], v[74:75], 0, s[20:21]
	v_lshl_add_u64 v[74:75], v[74:75], 0, v[178:179]
	s_waitcnt lgkmcnt(0)
	global_store_dwordx4 v[74:75], v[66:69], off sc1 nt
	s_branch .LBB0_2346

.LBB0_2443:
	v_mad_i64_i32 v[74:75], s[28:29], v74, s10, 0
	v_lshl_add_u64 v[74:75], v[74:75], 1, s[26:27]
	s_ashr_i32 s21, s20, 31
	v_lshl_add_u64 v[74:75], s[20:21], 1, v[74:75]
	v_lshlrev_b32_e32 v70, 1, v195
	v_lshl_add_u64 v[74:75], v[74:75], 0, v[70:71]
	s_waitcnt lgkmcnt(0)
	global_store_dwordx4 v[74:75], v[66:69], off sc1 nt
	ds_read_b128 v[66:69], v73 offset:8448
	s_cmp_lt_i32 s22, 1
	v_add_u32_e32 v74, s23, v207
	s_cbranch_scc1 .LBB0_2447
	s_cmp_eq_u32 s22, 1
	s_mov_b64 s[28:29], -1
	s_cbranch_scc0 .LBB0_2446
	v_lshlrev_b32_e32 v75, 2, v74
	v_lshrrev_b32_e32 v76, 1, v74
	v_and_b32_e32 v75, 16, v75
	v_and_b32_e32 v76, 12, v76
	v_and_b32_e32 v77, 0xffffffe3, v74
	v_or3_b32 v75, v75, v77, v76
	s_mov_b64 s[28:29], 0

.LBB0_2451:
	v_mad_i64_i32 v[74:75], s[28:29], v75, s10, 0
	v_lshl_add_u64 v[74:75], v[74:75], 1, s[26:27]
	v_lshl_add_u64 v[74:75], s[20:21], 1, v[74:75]
	v_lshl_add_u64 v[74:75], v[74:75], 0, v[70:71]
	s_waitcnt lgkmcnt(0)
	global_store_dwordx4 v[74:75], v[66:69], off sc1 nt
	ds_read_b128 v[66:69], v73 offset:16896
	s_cmp_lt_i32 s22, 1
	v_add_u32_e32 v74, s23, v213
	s_cbranch_scc1 .LBB0_2455
	s_cmp_eq_u32 s22, 1
	s_mov_b64 s[28:29], -1
	s_cbranch_scc0 .LBB0_2454
	v_lshlrev_b32_e32 v75, 2, v74
	v_lshrrev_b32_e32 v76, 1, v74
	v_and_b32_e32 v75, 16, v75
	v_and_b32_e32 v76, 12, v76
	v_and_b32_e32 v77, 0xffffffe3, v74
	v_or3_b32 v75, v75, v77, v76
	s_mov_b64 s[28:29], 0

.LBB0_2459:
	v_mad_i64_i32 v[74:75], s[28:29], v75, s10, 0
	v_lshl_add_u64 v[74:75], v[74:75], 1, s[26:27]
	v_lshl_add_u64 v[74:75], s[20:21], 1, v[74:75]
	v_lshl_add_u64 v[74:75], v[74:75], 0, v[70:71]
	s_waitcnt lgkmcnt(0)
	global_store_dwordx4 v[74:75], v[66:69], off sc1 nt
	ds_read_b128 v[66:69], v73 offset:25344
	s_cmp_lt_i32 s22, 1
	v_add_u32_e32 v74, s23, v208
	s_cbranch_scc1 .LBB0_2463
	s_cmp_eq_u32 s22, 1
	s_mov_b64 s[28:29], -1
	s_cbranch_scc0 .LBB0_2462
	v_lshlrev_b32_e32 v75, 2, v74
	v_lshrrev_b32_e32 v76, 1, v74
	v_and_b32_e32 v75, 16, v75
	v_and_b32_e32 v76, 12, v76
	v_and_b32_e32 v77, 0xffffffe3, v74
	v_or3_b32 v75, v75, v77, v76
	s_mov_b64 s[28:29], 0

.LBB0_2467:
	v_mad_i64_i32 v[74:75], s[28:29], v75, s10, 0
	v_lshl_add_u64 v[74:75], v[74:75], 1, s[26:27]
	v_lshl_add_u64 v[74:75], s[20:21], 1, v[74:75]
	v_lshl_add_u64 v[74:75], v[74:75], 0, v[70:71]
	s_waitcnt lgkmcnt(0)
	global_store_dwordx4 v[74:75], v[66:69], off sc1 nt
	ds_read_b128 v[66:69], v73 offset:33792
	s_cmp_lt_i32 s22, 1
	v_add_u32_e32 v74, s23, v209
	s_cbranch_scc1 .LBB0_2471
	s_cmp_eq_u32 s22, 1
	s_mov_b64 s[28:29], -1
	s_cbranch_scc0 .LBB0_2470
	v_lshlrev_b32_e32 v75, 2, v74
	v_lshrrev_b32_e32 v76, 1, v74
	v_and_b32_e32 v75, 16, v75
	v_and_b32_e32 v76, 12, v76
	v_and_b32_e32 v77, 0xffffffe3, v74
	v_or3_b32 v75, v75, v77, v76
	s_mov_b64 s[28:29], 0

.LBB0_2475:
	v_mad_i64_i32 v[74:75], s[28:29], v75, s10, 0
	v_lshl_add_u64 v[74:75], v[74:75], 1, s[26:27]
	v_lshl_add_u64 v[74:75], s[20:21], 1, v[74:75]
	v_lshl_add_u64 v[74:75], v[74:75], 0, v[70:71]
	s_waitcnt lgkmcnt(0)
	global_store_dwordx4 v[74:75], v[66:69], off sc1 nt
	ds_read_b128 v[66:69], v73 offset:42240
	s_cmp_lt_i32 s22, 1
	v_add_u32_e32 v74, s23, v210
	s_cbranch_scc1 .LBB0_2479
	s_cmp_eq_u32 s22, 1
	s_mov_b64 s[28:29], -1
	s_cbranch_scc0 .LBB0_2478
	v_lshlrev_b32_e32 v75, 2, v74
	v_lshrrev_b32_e32 v76, 1, v74
	v_and_b32_e32 v75, 16, v75
	v_and_b32_e32 v76, 12, v76
	v_and_b32_e32 v77, 0xffffffe3, v74
	v_or3_b32 v75, v75, v77, v76
	s_mov_b64 s[28:29], 0

.LBB0_2483:
	v_mad_i64_i32 v[74:75], s[28:29], v75, s10, 0
	v_lshl_add_u64 v[74:75], v[74:75], 1, s[26:27]
	v_lshl_add_u64 v[74:75], s[20:21], 1, v[74:75]
	v_lshl_add_u64 v[74:75], v[74:75], 0, v[70:71]
	s_waitcnt lgkmcnt(0)
	global_store_dwordx4 v[74:75], v[66:69], off sc1 nt
	ds_read_b128 v[66:69], v73 offset:50688
	s_cmp_lt_i32 s22, 1
	v_add_u32_e32 v74, s23, v211
	s_cbranch_scc1 .LBB0_2487
	s_cmp_eq_u32 s22, 1
	s_mov_b64 s[28:29], -1
	s_cbranch_scc0 .LBB0_2486
	v_lshlrev_b32_e32 v75, 2, v74
	v_lshrrev_b32_e32 v76, 1, v74
	v_and_b32_e32 v75, 16, v75
	v_and_b32_e32 v76, 12, v76
	v_and_b32_e32 v77, 0xffffffe3, v74
	v_or3_b32 v75, v75, v77, v76
	s_mov_b64 s[28:29], 0

.LBB0_2491:
	v_mad_i64_i32 v[74:75], s[28:29], v75, s10, 0
	v_lshl_add_u64 v[74:75], v[74:75], 1, s[26:27]
	v_lshl_add_u64 v[74:75], s[20:21], 1, v[74:75]
	v_lshl_add_u64 v[74:75], v[74:75], 0, v[70:71]
	s_waitcnt lgkmcnt(0)
	global_store_dwordx4 v[74:75], v[66:69], off sc1 nt
	ds_read_b128 v[66:69], v73 offset:59136
	s_cmp_lt_i32 s22, 1
	v_add_u32_e32 v73, s23, v212
	s_cbranch_scc1 .LBB0_2495
	s_cmp_eq_u32 s22, 1
	s_mov_b64 s[28:29], -1
	s_cbranch_scc0 .LBB0_2494
	v_lshlrev_b32_e32 v74, 2, v73
	v_lshrrev_b32_e32 v75, 1, v73
	v_and_b32_e32 v74, 16, v74
	v_and_b32_e32 v75, 12, v75
	v_and_b32_e32 v76, 0xffffffe3, v73
	v_or3_b32 v74, v74, v76, v75
	s_mov_b64 s[28:29], 0

.LBB0_3183:
	v_mad_i64_i32 v[90:91], s[24:25], v89, s24, 0
	v_lshl_add_u64 v[90:91], v[90:91], 1, s[18:19]
	v_lshl_add_u64 v[90:91], s[16:17], 1, v[90:91]
	v_mov_b32_e32 v77, v71
	v_lshl_add_u64 v[76:77], v[90:91], 0, v[76:77]
	s_waitcnt lgkmcnt(0)
	global_store_dwordx4 v[76:77], v[66:69], off sc1 nt

.LBB0_3253:
	v_mov_b64_e32 v[90:91], s[18:19]
	v_mad_i64_i32 v[90:91], s[26:27], v77, s24, v[90:91]
	s_ashr_i32 s17, s16, 31
	v_lshl_add_u64 v[90:91], v[90:91], 0, s[16:17]
	v_lshl_add_u64 v[90:91], v[90:91], 0, v[72:73]
	s_waitcnt lgkmcnt(0)
	global_store_dwordx4 v[90:91], v[66:69], off sc1 nt
	ds_read_b128 v[66:69], v87 offset:16896
	s_cmp_lt_i32 s63, 1
	v_add_u32_e32 v77, 32, v76
	s_cbranch_scc1 .LBB0_3257
	s_cmp_eq_u32 s63, 1
	s_mov_b64 s[26:27], -1
	s_cbranch_scc0 .LBB0_3256
	v_lshlrev_b32_e32 v89, 2, v77
	v_lshrrev_b32_e32 v90, 1, v77
	v_and_b32_e32 v89, 16, v89
	v_and_b32_e32 v90, 12, v90
	v_and_b32_e32 v91, 0xffffffe3, v77
	v_or3_b32 v89, v89, v91, v90
	s_mov_b64 s[26:27], 0

.LBB0_3261:
	v_mov_b64_e32 v[90:91], s[18:19]
	v_mad_i64_i32 v[90:91], s[26:27], v89, s24, v[90:91]
	v_lshl_add_u64 v[90:91], v[90:91], 0, s[16:17]
	v_lshl_add_u64 v[90:91], v[90:91], 0, v[72:73]
	s_waitcnt lgkmcnt(0)
	global_store_dwordx4 v[90:91], v[66:69], off sc1 nt
	ds_read_b128 v[66:69], v87 offset:33792
	s_cmp_lt_i32 s63, 1
	v_add_u32_e32 v77, s64, v81
	s_cbranch_scc1 .LBB0_3265
	s_cmp_eq_u32 s63, 1
	s_mov_b64 s[26:27], -1
	s_cbranch_scc0 .LBB0_3264
	v_lshlrev_b32_e32 v89, 2, v77
	v_lshrrev_b32_e32 v90, 1, v77
	v_and_b32_e32 v89, 16, v89
	v_and_b32_e32 v90, 12, v90
	v_and_b32_e32 v91, 0xffffffe3, v77
	v_or3_b32 v89, v89, v91, v90
	s_mov_b64 s[26:27], 0

.LBB0_3269:
	v_mov_b64_e32 v[90:91], s[18:19]
	v_mad_i64_i32 v[90:91], s[26:27], v89, s24, v[90:91]
	v_lshl_add_u64 v[90:91], v[90:91], 0, s[16:17]
	v_lshl_add_u64 v[90:91], v[90:91], 0, v[72:73]
	s_waitcnt lgkmcnt(0)
	global_store_dwordx4 v[90:91], v[66:69], off sc1 nt
	ds_read_b128 v[66:69], v87 offset:50688
	s_cmp_lt_i32 s63, 1
	v_add_u32_e32 v76, 0x60, v76
	s_cbranch_scc1 .LBB0_3273
	s_cmp_eq_u32 s63, 1
	s_mov_b64 s[26:27], -1
	s_cbranch_scc0 .LBB0_3272
	v_lshlrev_b32_e32 v77, 2, v76
	v_lshrrev_b32_e32 v89, 1, v76
	v_and_b32_e32 v77, 16, v77
	v_and_b32_e32 v89, 12, v89
	v_and_b32_e32 v90, 0xffffffe3, v76
	v_or3_b32 v77, v77, v90, v89
	s_mov_b64 s[26:27], 0

.LBB0_3277:
	v_mov_b64_e32 v[90:91], s[18:19]
	v_mad_i64_i32 v[76:77], s[26:27], v77, s24, v[90:91]
	v_lshl_add_u64 v[76:77], v[76:77], 0, s[16:17]
	v_lshl_add_u64 v[76:77], v[76:77], 0, v[72:73]
	s_waitcnt lgkmcnt(0)
	global_store_dwordx4 v[76:77], v[66:69], off sc1 nt
	s_branch .LBB0_3184

.LBB0_3286:
	v_mad_i64_i32 v[76:77], s[26:27], v76, s24, 0
	v_lshl_add_u64 v[76:77], v[76:77], 1, s[18:19]
	s_ashr_i32 s17, s16, 31
	v_lshl_add_u64 v[90:91], s[16:17], 1, v[76:77]
	v_lshlrev_b32_e32 v76, 1, v74
	v_mov_b32_e32 v77, v71
	v_lshl_add_u64 v[90:91], v[90:91], 0, v[76:77]
	s_waitcnt lgkmcnt(0)
	global_store_dwordx4 v[90:91], v[66:69], off sc1 nt
	ds_read_b128 v[66:69], v88 offset:8448
	s_cmp_lt_i32 s63, 1
	v_add_u32_e32 v77, 16, v89
	s_cbranch_scc1 .LBB0_3290
	s_cmp_eq_u32 s63, 1
	s_mov_b64 s[26:27], -1
	s_cbranch_scc0 .LBB0_3289
	v_lshlrev_b32_e32 v90, 2, v77
	v_lshrrev_b32_e32 v91, 1, v77
	v_and_b32_e32 v90, 16, v90
	v_and_b32_e32 v91, 12, v91
	v_and_b32_e32 v92, 0xffffffe3, v77
	v_or3_b32 v90, v90, v92, v91
	s_mov_b64 s[26:27], 0

.LBB0_3294:
	v_mad_i64_i32 v[90:91], s[26:27], v90, s24, 0
	v_lshl_add_u64 v[90:91], v[90:91], 1, s[18:19]
	v_lshl_add_u64 v[90:91], s[16:17], 1, v[90:91]
	v_mov_b32_e32 v77, v71
	v_lshl_add_u64 v[90:91], v[90:91], 0, v[76:77]
	s_waitcnt lgkmcnt(0)
	global_store_dwordx4 v[90:91], v[66:69], off sc1 nt
	ds_read_b128 v[66:69], v88 offset:16896
	s_cmp_lt_i32 s63, 1
	v_add_u32_e32 v77, s64, v82
	s_cbranch_scc1 .LBB0_3298
	s_cmp_eq_u32 s63, 1
	s_mov_b64 s[26:27], -1
	s_cbranch_scc0 .LBB0_3297
	v_lshlrev_b32_e32 v90, 2, v77
	v_lshrrev_b32_e32 v91, 1, v77
	v_and_b32_e32 v90, 16, v90
	v_and_b32_e32 v91, 12, v91
	v_and_b32_e32 v92, 0xffffffe3, v77
	v_or3_b32 v90, v90, v92, v91
	s_mov_b64 s[26:27], 0

.LBB0_3302:
	v_mad_i64_i32 v[90:91], s[26:27], v90, s24, 0
	v_lshl_add_u64 v[90:91], v[90:91], 1, s[18:19]
	v_lshl_add_u64 v[90:91], s[16:17], 1, v[90:91]
	v_mov_b32_e32 v77, v71
	v_lshl_add_u64 v[90:91], v[90:91], 0, v[76:77]
	s_waitcnt lgkmcnt(0)
	global_store_dwordx4 v[90:91], v[66:69], off sc1 nt
	ds_read_b128 v[66:69], v88 offset:25344
	s_cmp_lt_i32 s63, 1
	v_add_u32_e32 v77, 48, v89
	s_cbranch_scc1 .LBB0_3306
	s_cmp_eq_u32 s63, 1
	s_mov_b64 s[26:27], -1
	s_cbranch_scc0 .LBB0_3305
	v_lshlrev_b32_e32 v90, 2, v77
	v_lshrrev_b32_e32 v91, 1, v77
	v_and_b32_e32 v90, 16, v90
	v_and_b32_e32 v91, 12, v91
	v_and_b32_e32 v92, 0xffffffe3, v77
	v_or3_b32 v90, v90, v92, v91
	s_mov_b64 s[26:27], 0

.LBB0_3310:
	v_mad_i64_i32 v[90:91], s[26:27], v90, s24, 0
	v_lshl_add_u64 v[90:91], v[90:91], 1, s[18:19]
	v_lshl_add_u64 v[90:91], s[16:17], 1, v[90:91]
	v_mov_b32_e32 v77, v71
	v_lshl_add_u64 v[90:91], v[90:91], 0, v[76:77]
	s_waitcnt lgkmcnt(0)
	global_store_dwordx4 v[90:91], v[66:69], off sc1 nt
	ds_read_b128 v[66:69], v88 offset:33792
	s_cmp_lt_i32 s63, 1
	v_add_u32_e32 v77, s64, v83
	s_cbranch_scc1 .LBB0_3314
	s_cmp_eq_u32 s63, 1
	s_mov_b64 s[26:27], -1
	s_cbranch_scc0 .LBB0_3313
	v_lshlrev_b32_e32 v90, 2, v77
	v_lshrrev_b32_e32 v91, 1, v77
	v_and_b32_e32 v90, 16, v90
	v_and_b32_e32 v91, 12, v91
	v_and_b32_e32 v92, 0xffffffe3, v77
	v_or3_b32 v90, v90, v92, v91
	s_mov_b64 s[26:27], 0

.LBB0_3318:
	v_mad_i64_i32 v[90:91], s[26:27], v90, s24, 0
	v_lshl_add_u64 v[90:91], v[90:91], 1, s[18:19]
	v_lshl_add_u64 v[90:91], s[16:17], 1, v[90:91]
	v_mov_b32_e32 v77, v71
	v_lshl_add_u64 v[90:91], v[90:91], 0, v[76:77]
	s_waitcnt lgkmcnt(0)
	global_store_dwordx4 v[90:91], v[66:69], off sc1 nt
	ds_read_b128 v[66:69], v88 offset:42240
	s_cmp_lt_i32 s63, 1
	v_add_u32_e32 v77, 0x50, v89
	s_cbranch_scc1 .LBB0_3322
	s_cmp_eq_u32 s63, 1
	s_mov_b64 s[26:27], -1
	s_cbranch_scc0 .LBB0_3321
	v_lshlrev_b32_e32 v90, 2, v77
	v_lshrrev_b32_e32 v91, 1, v77
	v_and_b32_e32 v90, 16, v90
	v_and_b32_e32 v91, 12, v91
	v_and_b32_e32 v92, 0xffffffe3, v77
	v_or3_b32 v90, v90, v92, v91
	s_mov_b64 s[26:27], 0

.LBB0_3326:
	v_mad_i64_i32 v[90:91], s[26:27], v90, s24, 0
	v_lshl_add_u64 v[90:91], v[90:91], 1, s[18:19]
	v_lshl_add_u64 v[90:91], s[16:17], 1, v[90:91]
	v_mov_b32_e32 v77, v71
	v_lshl_add_u64 v[90:91], v[90:91], 0, v[76:77]
	s_waitcnt lgkmcnt(0)
	global_store_dwordx4 v[90:91], v[66:69], off sc1 nt
	ds_read_b128 v[66:69], v88 offset:50688
	s_cmp_lt_i32 s63, 1
	v_add_u32_e32 v77, s64, v84
	s_cbranch_scc1 .LBB0_3330
	s_cmp_eq_u32 s63, 1
	s_mov_b64 s[26:27], -1
	s_cbranch_scc0 .LBB0_3329
	v_lshlrev_b32_e32 v90, 2, v77
	v_lshrrev_b32_e32 v91, 1, v77
	v_and_b32_e32 v90, 16, v90
	v_and_b32_e32 v91, 12, v91
	v_and_b32_e32 v92, 0xffffffe3, v77
	v_or3_b32 v90, v90, v92, v91
	s_mov_b64 s[26:27], 0

.LBB0_3334:
	v_mad_i64_i32 v[90:91], s[26:27], v90, s24, 0
	v_lshl_add_u64 v[90:91], v[90:91], 1, s[18:19]
	v_lshl_add_u64 v[90:91], s[16:17], 1, v[90:91]
	v_mov_b32_e32 v77, v71
	v_lshl_add_u64 v[90:91], v[90:91], 0, v[76:77]
	s_waitcnt lgkmcnt(0)
	global_store_dwordx4 v[90:91], v[66:69], off sc1 nt
	ds_read_b128 v[66:69], v88 offset:59136
	s_cmp_lt_i32 s63, 1
	v_add_u32_e32 v77, 0x70, v89
	s_cbranch_scc1 .LBB0_3338
	s_cmp_eq_u32 s63, 1
	s_mov_b64 s[26:27], -1
	s_cbranch_scc0 .LBB0_3337
	v_lshlrev_b32_e32 v89, 2, v77
	v_lshrrev_b32_e32 v90, 1, v77
	v_and_b32_e32 v89, 16, v89
	v_and_b32_e32 v90, 12, v90
	v_and_b32_e32 v91, 0xffffffe3, v77
	v_or3_b32 v89, v89, v91, v90
	s_mov_b64 s[26:27], 0

.LBB0_3425:
	v_mad_i64_i32 v[90:91], s[22:23], v89, s24, 0
	v_lshl_add_u64 v[90:91], v[90:91], 1, s[16:17]
	v_lshl_add_u64 v[90:91], s[14:15], 1, v[90:91]
	v_mov_b32_e32 v77, v71
	v_lshl_add_u64 v[76:77], v[90:91], 0, v[76:77]
	s_waitcnt lgkmcnt(0)
	global_store_dwordx4 v[76:77], v[66:69], off sc1 nt

.LBB0_3495:
	v_mov_b64_e32 v[90:91], s[16:17]
	v_mad_i64_i32 v[90:91], s[22:23], v77, s24, v[90:91]
	s_ashr_i32 s15, s14, 31
	v_lshl_add_u64 v[90:91], v[90:91], 0, s[14:15]
	v_lshl_add_u64 v[90:91], v[90:91], 0, v[72:73]
	s_waitcnt lgkmcnt(0)
	global_store_dwordx4 v[90:91], v[66:69], off sc1 nt
	ds_read_b128 v[66:69], v87 offset:16896
	s_cmp_lt_i32 s60, 1
	v_add_u32_e32 v77, 32, v76
	s_cbranch_scc1 .LBB0_3499
	s_cmp_eq_u32 s60, 1
	s_mov_b64 s[22:23], -1
	s_cbranch_scc0 .LBB0_3498
	v_lshlrev_b32_e32 v89, 2, v77
	v_lshrrev_b32_e32 v90, 1, v77
	v_and_b32_e32 v89, 16, v89
	v_and_b32_e32 v90, 12, v90
	v_and_b32_e32 v91, 0xffffffe3, v77
	v_or3_b32 v89, v89, v91, v90
	s_mov_b64 s[22:23], 0

.LBB0_3503:
	v_mov_b64_e32 v[90:91], s[16:17]
	v_mad_i64_i32 v[90:91], s[22:23], v89, s24, v[90:91]
	v_lshl_add_u64 v[90:91], v[90:91], 0, s[14:15]
	v_lshl_add_u64 v[90:91], v[90:91], 0, v[72:73]
	s_waitcnt lgkmcnt(0)
	global_store_dwordx4 v[90:91], v[66:69], off sc1 nt
	ds_read_b128 v[66:69], v87 offset:33792
	s_cmp_lt_i32 s60, 1
	v_add_u32_e32 v77, s61, v81
	s_cbranch_scc1 .LBB0_3507
	s_cmp_eq_u32 s60, 1
	s_mov_b64 s[22:23], -1
	s_cbranch_scc0 .LBB0_3506
	v_lshlrev_b32_e32 v89, 2, v77
	v_lshrrev_b32_e32 v90, 1, v77
	v_and_b32_e32 v89, 16, v89
	v_and_b32_e32 v90, 12, v90
	v_and_b32_e32 v91, 0xffffffe3, v77
	v_or3_b32 v89, v89, v91, v90
	s_mov_b64 s[22:23], 0

.LBB0_3511:
	v_mov_b64_e32 v[90:91], s[16:17]
	v_mad_i64_i32 v[90:91], s[22:23], v89, s24, v[90:91]
	v_lshl_add_u64 v[90:91], v[90:91], 0, s[14:15]
	v_lshl_add_u64 v[90:91], v[90:91], 0, v[72:73]
	s_waitcnt lgkmcnt(0)
	global_store_dwordx4 v[90:91], v[66:69], off sc1 nt
	ds_read_b128 v[66:69], v87 offset:50688
	s_cmp_lt_i32 s60, 1
	v_add_u32_e32 v76, 0x60, v76
	s_cbranch_scc1 .LBB0_3515
	s_cmp_eq_u32 s60, 1
	s_mov_b64 s[22:23], -1
	s_cbranch_scc0 .LBB0_3514
	v_lshlrev_b32_e32 v77, 2, v76
	v_lshrrev_b32_e32 v89, 1, v76
	v_and_b32_e32 v77, 16, v77
	v_and_b32_e32 v89, 12, v89
	v_and_b32_e32 v90, 0xffffffe3, v76
	v_or3_b32 v77, v77, v90, v89
	s_mov_b64 s[22:23], 0

.LBB0_3519:
	v_mov_b64_e32 v[90:91], s[16:17]
	v_mad_i64_i32 v[76:77], s[22:23], v77, s24, v[90:91]
	v_lshl_add_u64 v[76:77], v[76:77], 0, s[14:15]
	v_lshl_add_u64 v[76:77], v[76:77], 0, v[72:73]
	s_waitcnt lgkmcnt(0)
	global_store_dwordx4 v[76:77], v[66:69], off sc1 nt
	s_branch .LBB0_3426

.LBB0_3528:
	v_mad_i64_i32 v[76:77], s[22:23], v76, s24, 0
	v_lshl_add_u64 v[76:77], v[76:77], 1, s[16:17]
	s_ashr_i32 s15, s14, 31
	v_lshl_add_u64 v[90:91], s[14:15], 1, v[76:77]
	v_lshlrev_b32_e32 v76, 1, v74
	v_mov_b32_e32 v77, v71
	v_lshl_add_u64 v[90:91], v[90:91], 0, v[76:77]
	s_waitcnt lgkmcnt(0)
	global_store_dwordx4 v[90:91], v[66:69], off sc1 nt
	ds_read_b128 v[66:69], v88 offset:8448
	s_cmp_lt_i32 s60, 1
	v_add_u32_e32 v77, 16, v89
	s_cbranch_scc1 .LBB0_3532
	s_cmp_eq_u32 s60, 1
	s_mov_b64 s[22:23], -1
	s_cbranch_scc0 .LBB0_3531
	v_lshlrev_b32_e32 v90, 2, v77
	v_lshrrev_b32_e32 v91, 1, v77
	v_and_b32_e32 v90, 16, v90
	v_and_b32_e32 v91, 12, v91
	v_and_b32_e32 v92, 0xffffffe3, v77
	v_or3_b32 v90, v90, v92, v91
	s_mov_b64 s[22:23], 0

.LBB0_3536:
	v_mad_i64_i32 v[90:91], s[22:23], v90, s24, 0
	v_lshl_add_u64 v[90:91], v[90:91], 1, s[16:17]
	v_lshl_add_u64 v[90:91], s[14:15], 1, v[90:91]
	v_mov_b32_e32 v77, v71
	v_lshl_add_u64 v[90:91], v[90:91], 0, v[76:77]
	s_waitcnt lgkmcnt(0)
	global_store_dwordx4 v[90:91], v[66:69], off sc1 nt
	ds_read_b128 v[66:69], v88 offset:16896
	s_cmp_lt_i32 s60, 1
	v_add_u32_e32 v77, s61, v82
	s_cbranch_scc1 .LBB0_3540
	s_cmp_eq_u32 s60, 1
	s_mov_b64 s[22:23], -1
	s_cbranch_scc0 .LBB0_3539
	v_lshlrev_b32_e32 v90, 2, v77
	v_lshrrev_b32_e32 v91, 1, v77
	v_and_b32_e32 v90, 16, v90
	v_and_b32_e32 v91, 12, v91
	v_and_b32_e32 v92, 0xffffffe3, v77
	v_or3_b32 v90, v90, v92, v91
	s_mov_b64 s[22:23], 0

.LBB0_3544:
	v_mad_i64_i32 v[90:91], s[22:23], v90, s24, 0
	v_lshl_add_u64 v[90:91], v[90:91], 1, s[16:17]
	v_lshl_add_u64 v[90:91], s[14:15], 1, v[90:91]
	v_mov_b32_e32 v77, v71
	v_lshl_add_u64 v[90:91], v[90:91], 0, v[76:77]
	s_waitcnt lgkmcnt(0)
	global_store_dwordx4 v[90:91], v[66:69], off sc1 nt
	ds_read_b128 v[66:69], v88 offset:25344
	s_cmp_lt_i32 s60, 1
	v_add_u32_e32 v77, 48, v89
	s_cbranch_scc1 .LBB0_3548
	s_cmp_eq_u32 s60, 1
	s_mov_b64 s[22:23], -1
	s_cbranch_scc0 .LBB0_3547
	v_lshlrev_b32_e32 v90, 2, v77
	v_lshrrev_b32_e32 v91, 1, v77
	v_and_b32_e32 v90, 16, v90
	v_and_b32_e32 v91, 12, v91
	v_and_b32_e32 v92, 0xffffffe3, v77
	v_or3_b32 v90, v90, v92, v91
	s_mov_b64 s[22:23], 0

.LBB0_3552:
	v_mad_i64_i32 v[90:91], s[22:23], v90, s24, 0
	v_lshl_add_u64 v[90:91], v[90:91], 1, s[16:17]
	v_lshl_add_u64 v[90:91], s[14:15], 1, v[90:91]
	v_mov_b32_e32 v77, v71
	v_lshl_add_u64 v[90:91], v[90:91], 0, v[76:77]
	s_waitcnt lgkmcnt(0)
	global_store_dwordx4 v[90:91], v[66:69], off sc1 nt
	ds_read_b128 v[66:69], v88 offset:33792
	s_cmp_lt_i32 s60, 1
	v_add_u32_e32 v77, s61, v83
	s_cbranch_scc1 .LBB0_3556
	s_cmp_eq_u32 s60, 1
	s_mov_b64 s[22:23], -1
	s_cbranch_scc0 .LBB0_3555
	v_lshlrev_b32_e32 v90, 2, v77
	v_lshrrev_b32_e32 v91, 1, v77
	v_and_b32_e32 v90, 16, v90
	v_and_b32_e32 v91, 12, v91
	v_and_b32_e32 v92, 0xffffffe3, v77
	v_or3_b32 v90, v90, v92, v91
	s_mov_b64 s[22:23], 0

.LBB0_3560:
	v_mad_i64_i32 v[90:91], s[22:23], v90, s24, 0
	v_lshl_add_u64 v[90:91], v[90:91], 1, s[16:17]
	v_lshl_add_u64 v[90:91], s[14:15], 1, v[90:91]
	v_mov_b32_e32 v77, v71
	v_lshl_add_u64 v[90:91], v[90:91], 0, v[76:77]
	s_waitcnt lgkmcnt(0)
	global_store_dwordx4 v[90:91], v[66:69], off sc1 nt
	ds_read_b128 v[66:69], v88 offset:42240
	s_cmp_lt_i32 s60, 1
	v_add_u32_e32 v77, 0x50, v89
	s_cbranch_scc1 .LBB0_3564
	s_cmp_eq_u32 s60, 1
	s_mov_b64 s[22:23], -1
	s_cbranch_scc0 .LBB0_3563
	v_lshlrev_b32_e32 v90, 2, v77
	v_lshrrev_b32_e32 v91, 1, v77
	v_and_b32_e32 v90, 16, v90
	v_and_b32_e32 v91, 12, v91
	v_and_b32_e32 v92, 0xffffffe3, v77
	v_or3_b32 v90, v90, v92, v91
	s_mov_b64 s[22:23], 0

.LBB0_3568:
	v_mad_i64_i32 v[90:91], s[22:23], v90, s24, 0
	v_lshl_add_u64 v[90:91], v[90:91], 1, s[16:17]
	v_lshl_add_u64 v[90:91], s[14:15], 1, v[90:91]
	v_mov_b32_e32 v77, v71
	v_lshl_add_u64 v[90:91], v[90:91], 0, v[76:77]
	s_waitcnt lgkmcnt(0)
	global_store_dwordx4 v[90:91], v[66:69], off sc1 nt
	ds_read_b128 v[66:69], v88 offset:50688
	s_cmp_lt_i32 s60, 1
	v_add_u32_e32 v77, s61, v84
	s_cbranch_scc1 .LBB0_3572
	s_cmp_eq_u32 s60, 1
	s_mov_b64 s[22:23], -1
	s_cbranch_scc0 .LBB0_3571
	v_lshlrev_b32_e32 v90, 2, v77
	v_lshrrev_b32_e32 v91, 1, v77
	v_and_b32_e32 v90, 16, v90
	v_and_b32_e32 v91, 12, v91
	v_and_b32_e32 v92, 0xffffffe3, v77
	v_or3_b32 v90, v90, v92, v91
	s_mov_b64 s[22:23], 0

.LBB0_3576:
	v_mad_i64_i32 v[90:91], s[22:23], v90, s24, 0
	v_lshl_add_u64 v[90:91], v[90:91], 1, s[16:17]
	v_lshl_add_u64 v[90:91], s[14:15], 1, v[90:91]
	v_mov_b32_e32 v77, v71
	v_lshl_add_u64 v[90:91], v[90:91], 0, v[76:77]
	s_waitcnt lgkmcnt(0)
	global_store_dwordx4 v[90:91], v[66:69], off sc1 nt
	ds_read_b128 v[66:69], v88 offset:59136
	s_cmp_lt_i32 s60, 1
	v_add_u32_e32 v77, 0x70, v89
	s_cbranch_scc1 .LBB0_3580
	s_cmp_eq_u32 s60, 1
	s_mov_b64 s[22:23], -1
	s_cbranch_scc0 .LBB0_3579
	v_lshlrev_b32_e32 v89, 2, v77
	v_lshrrev_b32_e32 v90, 1, v77
	v_and_b32_e32 v89, 16, v89
	v_and_b32_e32 v90, 12, v90
	v_and_b32_e32 v91, 0xffffffe3, v77
	v_or3_b32 v89, v89, v91, v90
	s_mov_b64 s[22:23], 0

.LBB0_3852:
	v_mov_b32_e32 v34, v22
	v_mov_b32_e32 v35, v22
	v_pk_mul_f32 v[22:23], v[22:23], v[24:25]
	s_waitcnt vmcnt(2)
	v_lshlrev_b32_e32 v28, 16, v42
	v_and_b32_e32 v29, 0xffff0000, v42
	v_pk_mul_f32 v[26:27], v[34:35], v[26:27]
	v_mov_b32_e32 v24, v20
	v_mov_b32_e32 v25, v20
	v_pk_fma_f32 v[0:1], v[20:21], v[0:1], v[22:23]
	v_lshlrev_b32_e32 v30, 16, v43
	v_and_b32_e32 v31, 0xffff0000, v43
	v_pk_fma_f32 v[2:3], v[24:25], v[2:3], v[26:27]
	s_waitcnt vmcnt(1)
	v_pk_fma_f32 v[0:1], v[4:5], v[0:1], v[28:29]
	v_add_co_u32_e32 v4, vcc, 0x1000, v32
	s_add_i32 s4, s4, s16
	v_pk_fma_f32 v[2:3], v[6:7], v[2:3], v[30:31]
	v_addc_co_u32_e32 v5, vcc, 0, v33, vcc
	s_cmpk_lt_i32 s4, 0x2000
	global_store_dwordx4 v[4:5], v[0:3], off offset:3072 sc1 nt
	s_cbranch_scc0 .LBB0_3917

.LBB0_3861:
	global_load_dwordx2 v[46:47], v[28:29], off offset:512
	global_load_dwordx2 v[44:45], v[30:31], off offset:512
	global_load_dwordx2 v[34:35], v[26:27], off offset:512
	global_load_dwordx4 v[4:7], v[24:25], off offset:1024
	v_pk_mul_f32 v[42:43], v[22:23], v[42:43] op_sel_hi:[0,1]
	v_pk_mul_f32 v[40:41], v[22:23], v[40:41] op_sel_hi:[0,1]
	s_lshl_b64 s[2:3], s[4:5], 11
	v_lshlrev_b32_e32 v48, 16, v32
	v_and_b32_e32 v49, 0xffff0000, v32
	v_lshlrev_b32_e32 v52, 16, v33
	v_and_b32_e32 v53, 0xffff0000, v33
	v_pk_fma_f32 v[38:39], v[20:21], v[38:39], v[42:43] op_sel_hi:[0,1,1]
	v_pk_fma_f32 v[36:37], v[20:21], v[36:37], v[40:41] op_sel_hi:[0,1,1]
	v_lshl_add_u64 v[32:33], s[2:3], 2, v[16:17]
	v_pk_fma_f32 v[0:1], v[0:1], v[36:37], v[48:49]
	v_pk_fma_f32 v[2:3], v[2:3], v[38:39], v[52:53]
	global_store_dwordx4 v[32:33], v[0:3], off sc1 nt
	ds_read_b32 v0, v50 offset:516
	ds_read_b32 v1, v51 offset:516
	s_waitcnt lgkmcnt(1)
	v_readfirstlane_b32 s3, v0
	s_cmp_lt_i32 s3, 0
	s_waitcnt lgkmcnt(0)
	v_readfirstlane_b32 s2, v1
	s_waitcnt vmcnt(4)
	v_lshlrev_b32_e32 v38, 16, v46
	v_and_b32_e32 v39, 0xffff0000, v46
	v_lshlrev_b32_e32 v40, 16, v47
	v_and_b32_e32 v41, 0xffff0000, v47
	s_cbranch_scc1 .LBB0_3865
	s_and_b64 vcc, exec, s[0:1]
	s_cbranch_vccnz .LBB0_3865
	s_mul_i32 s5, s9, s3
	s_mul_hi_u32 s24, s8, s3
	s_add_i32 s5, s24, s5
	s_mul_i32 s3, s8, s3
	s_lshl_b32 s24, s14, 2
	s_add_u32 s24, s3, s24
	s_addc_u32 s25, s5, 0
	v_lshl_add_u64 v[0:1], v[18:19], 0, s[24:25]
	s_mov_b32 s3, s6

.LBB0_3869:
	global_load_dwordx2 v[48:49], v[28:29], off offset:1024
	global_load_dwordx2 v[46:47], v[30:31], off offset:1024
	global_load_dwordx2 v[36:37], v[26:27], off offset:1024
	global_load_dwordx4 v[0:3], v[24:25], off offset:2048
	v_mov_b32_e32 v23, v22
	v_mov_b32_e32 v54, v22
	v_mov_b32_e32 v55, v22
	v_mov_b32_e32 v21, v20
	v_mov_b32_e32 v56, v20
	v_mov_b32_e32 v57, v20
	v_pk_mul_f32 v[44:45], v[54:55], v[44:45]
	v_pk_mul_f32 v[42:43], v[22:23], v[42:43]
	s_waitcnt vmcnt(6)
	v_lshlrev_b32_e32 v52, 16, v34
	v_and_b32_e32 v53, 0xffff0000, v34
	v_lshlrev_b32_e32 v34, 16, v35
	v_and_b32_e32 v35, 0xffff0000, v35
	v_pk_fma_f32 v[40:41], v[56:57], v[40:41], v[44:45]
	v_pk_fma_f32 v[38:39], v[20:21], v[38:39], v[42:43]
	s_waitcnt vmcnt(5)
	v_pk_fma_f32 v[6:7], v[6:7], v[40:41], v[34:35]
	v_pk_fma_f32 v[4:5], v[4:5], v[38:39], v[52:53]
	global_store_dwordx4 v[32:33], v[4:7], off offset:1024 sc1 nt
	ds_read_b32 v4, v50 offset:520
	ds_read_b32 v5, v51 offset:520
	s_waitcnt lgkmcnt(1)
	v_readfirstlane_b32 s3, v4
	s_cmp_lt_i32 s3, 0
	s_waitcnt lgkmcnt(0)
	v_readfirstlane_b32 s2, v5
	s_waitcnt vmcnt(4)
	v_lshlrev_b32_e32 v38, 16, v48
	v_and_b32_e32 v39, 0xffff0000, v48
	v_lshlrev_b32_e32 v40, 16, v49
	v_and_b32_e32 v41, 0xffff0000, v49
	s_cbranch_scc1 .LBB0_3873
	s_and_b64 vcc, exec, s[0:1]
	s_cbranch_vccnz .LBB0_3873
	s_mul_i32 s5, s9, s3
	s_mul_hi_u32 s24, s8, s3
	s_add_i32 s5, s24, s5
	s_mul_i32 s3, s8, s3
	s_lshl_b32 s24, s14, 2
	s_add_u32 s24, s3, s24
	s_addc_u32 s25, s5, 0
	v_lshl_add_u64 v[4:5], v[18:19], 0, s[24:25]
	s_mov_b32 s3, s6

.LBB0_3877:
	global_load_dwordx2 v[48:49], v[28:29], off offset:1536
	global_load_dwordx2 v[46:47], v[30:31], off offset:1536
	global_load_dwordx2 v[34:35], v[26:27], off offset:1536
	global_load_dwordx4 v[4:7], v[24:25], off offset:3072
	v_mov_b32_e32 v54, v22
	v_mov_b32_e32 v55, v22
	v_pk_mul_f32 v[44:45], v[22:23], v[44:45]
	v_mov_b32_e32 v56, v20
	v_mov_b32_e32 v57, v20
	v_pk_mul_f32 v[42:43], v[54:55], v[42:43]
	s_waitcnt vmcnt(6)
	v_lshlrev_b32_e32 v52, 16, v36
	v_and_b32_e32 v53, 0xffff0000, v36
	v_lshlrev_b32_e32 v36, 16, v37
	v_and_b32_e32 v37, 0xffff0000, v37
	v_pk_fma_f32 v[38:39], v[20:21], v[38:39], v[44:45]
	v_pk_fma_f32 v[40:41], v[56:57], v[40:41], v[42:43]
	s_waitcnt vmcnt(5)
	v_pk_fma_f32 v[0:1], v[0:1], v[38:39], v[52:53]
	v_pk_fma_f32 v[2:3], v[2:3], v[40:41], v[36:37]
	global_store_dwordx4 v[32:33], v[0:3], off offset:2048 sc1 nt
	ds_read_b32 v0, v50 offset:524
	ds_read_b32 v1, v51 offset:524
	s_waitcnt lgkmcnt(1)
	v_readfirstlane_b32 s3, v0
	s_cmp_lt_i32 s3, 0
	s_waitcnt lgkmcnt(0)
	v_readfirstlane_b32 s2, v1
	s_waitcnt vmcnt(4)
	v_lshlrev_b32_e32 v38, 16, v48
	v_and_b32_e32 v39, 0xffff0000, v48
	v_lshlrev_b32_e32 v40, 16, v49
	v_and_b32_e32 v41, 0xffff0000, v49
	s_cbranch_scc1 .LBB0_3881
	s_and_b64 vcc, exec, s[0:1]
	s_cbranch_vccnz .LBB0_3881
	s_mul_i32 s5, s9, s3
	s_mul_hi_u32 s24, s8, s3
	s_add_i32 s5, s24, s5
	s_mul_i32 s3, s8, s3
	s_lshl_b32 s24, s14, 2
	s_add_u32 s24, s3, s24
	s_addc_u32 s25, s5, 0
	v_lshl_add_u64 v[0:1], v[18:19], 0, s[24:25]
	s_mov_b32 s3, s6

.LBB0_3885:
	v_add_co_u32_e32 v0, vcc, 0x1000, v24
	global_load_dwordx2 v[46:47], v[28:29], off offset:2048
	global_load_dwordx2 v[48:49], v[30:31], off offset:2048
	global_load_dwordx2 v[36:37], v[26:27], off offset:2048
	v_addc_co_u32_e32 v1, vcc, 0, v25, vcc
	global_load_dwordx4 v[0:3], v[0:1], off
	v_mov_b32_e32 v54, v22
	v_mov_b32_e32 v55, v22
	v_pk_mul_f32 v[44:45], v[22:23], v[44:45]
	v_mov_b32_e32 v56, v20
	v_mov_b32_e32 v57, v20
	v_pk_mul_f32 v[42:43], v[54:55], v[42:43]
	s_waitcnt vmcnt(6)
	v_lshlrev_b32_e32 v52, 16, v34
	v_and_b32_e32 v53, 0xffff0000, v34
	v_lshlrev_b32_e32 v34, 16, v35
	v_and_b32_e32 v35, 0xffff0000, v35
	v_pk_fma_f32 v[38:39], v[20:21], v[38:39], v[44:45]
	v_pk_fma_f32 v[40:41], v[56:57], v[40:41], v[42:43]
	s_waitcnt vmcnt(5)
	v_pk_fma_f32 v[4:5], v[4:5], v[38:39], v[52:53]
	v_pk_fma_f32 v[6:7], v[6:7], v[40:41], v[34:35]
	global_store_dwordx4 v[32:33], v[4:7], off offset:3072 sc1 nt
	ds_read_b32 v4, v50 offset:528
	ds_read_b32 v5, v51 offset:528
	s_waitcnt lgkmcnt(1)
	v_readfirstlane_b32 s3, v4
	s_cmp_lt_i32 s3, 0
	s_waitcnt lgkmcnt(0)
	v_readfirstlane_b32 s2, v5
	s_waitcnt vmcnt(4)
	v_lshlrev_b32_e32 v40, 16, v46
	v_and_b32_e32 v41, 0xffff0000, v46
	v_lshlrev_b32_e32 v42, 16, v47
	v_and_b32_e32 v43, 0xffff0000, v47
	s_cbranch_scc1 .LBB0_3889
	s_and_b64 vcc, exec, s[0:1]
	s_cbranch_vccnz .LBB0_3889
	s_mul_i32 s5, s9, s3
	s_mul_hi_u32 s24, s8, s3
	s_add_i32 s5, s24, s5
	s_mul_i32 s3, s8, s3
	s_lshl_b32 s24, s14, 2
	s_add_u32 s24, s3, s24
	s_addc_u32 s25, s5, 0
	v_lshl_add_u64 v[4:5], v[18:19], 0, s[24:25]
	s_mov_b32 s3, s6

.LBB0_3893:
	v_add_co_u32_e32 v34, vcc, s23, v32
	s_mov_b64 s[2:3], vcc
	v_add_co_u32_e32 v4, vcc, 0x1000, v24
	global_load_dwordx2 v[52:53], v[28:29], off offset:2560
	global_load_dwordx2 v[48:49], v[30:31], off offset:2560
	global_load_dwordx2 v[38:39], v[26:27], off offset:2560
	v_addc_co_u32_e32 v5, vcc, 0, v25, vcc
	global_load_dwordx4 v[4:7], v[4:5], off offset:1024
	v_mov_b32_e32 v56, v22
	v_mov_b32_e32 v57, v22
	v_pk_mul_f32 v[46:47], v[22:23], v[46:47]
	v_mov_b32_e32 v58, v20
	v_mov_b32_e32 v59, v20
	v_pk_mul_f32 v[44:45], v[56:57], v[44:45]
	s_waitcnt vmcnt(6)
	v_lshlrev_b32_e32 v54, 16, v36
	v_and_b32_e32 v55, 0xffff0000, v36
	v_lshlrev_b32_e32 v36, 16, v37
	v_and_b32_e32 v37, 0xffff0000, v37
	v_pk_fma_f32 v[40:41], v[20:21], v[40:41], v[46:47]
	v_pk_fma_f32 v[42:43], v[58:59], v[42:43], v[44:45]
	v_addc_co_u32_e64 v35, vcc, 0, v33, s[2:3]
	s_waitcnt vmcnt(5)
	v_pk_fma_f32 v[0:1], v[0:1], v[40:41], v[54:55]
	v_pk_fma_f32 v[2:3], v[2:3], v[42:43], v[36:37]
	global_store_dwordx4 v[34:35], v[0:3], off sc1 nt
	ds_read_b32 v0, v50 offset:532
	ds_read_b32 v1, v51 offset:532
	s_waitcnt lgkmcnt(1)
	v_readfirstlane_b32 s3, v0
	s_cmp_lt_i32 s3, 0
	s_waitcnt lgkmcnt(0)
	v_readfirstlane_b32 s2, v1
	s_waitcnt vmcnt(4)
	v_lshlrev_b32_e32 v40, 16, v52
	v_and_b32_e32 v41, 0xffff0000, v52
	v_lshlrev_b32_e32 v42, 16, v53
	v_and_b32_e32 v43, 0xffff0000, v53
	s_cbranch_scc1 .LBB0_3897
	s_and_b64 vcc, exec, s[0:1]
	s_cbranch_vccnz .LBB0_3897
	s_mul_i32 s5, s9, s3
	s_mul_hi_u32 s24, s8, s3
	s_add_i32 s5, s24, s5
	s_mul_i32 s3, s8, s3
	s_lshl_b32 s24, s14, 2
	s_add_u32 s24, s3, s24
	s_addc_u32 s25, s5, 0
	v_lshl_add_u64 v[0:1], v[18:19], 0, s[24:25]
	s_mov_b32 s3, s6

.LBB0_3901:
	v_add_co_u32_e32 v0, vcc, 0x1000, v24
	global_load_dwordx2 v[52:53], v[28:29], off offset:3072
	global_load_dwordx2 v[48:49], v[30:31], off offset:3072
	global_load_dwordx2 v[36:37], v[26:27], off offset:3072
	v_addc_co_u32_e32 v1, vcc, 0, v25, vcc
	global_load_dwordx4 v[0:3], v[0:1], off offset:2048
	v_mov_b32_e32 v56, v22
	v_mov_b32_e32 v57, v22
	v_pk_mul_f32 v[46:47], v[22:23], v[46:47]
	v_mov_b32_e32 v58, v20
	v_mov_b32_e32 v59, v20
	v_pk_mul_f32 v[44:45], v[56:57], v[44:45]
	s_waitcnt vmcnt(6)
	v_lshlrev_b32_e32 v54, 16, v38
	v_and_b32_e32 v55, 0xffff0000, v38
	v_lshlrev_b32_e32 v38, 16, v39
	v_and_b32_e32 v39, 0xffff0000, v39
	v_pk_fma_f32 v[40:41], v[20:21], v[40:41], v[46:47]
	v_pk_fma_f32 v[42:43], v[58:59], v[42:43], v[44:45]
	s_waitcnt vmcnt(5)
	v_pk_fma_f32 v[4:5], v[4:5], v[40:41], v[54:55]
	v_pk_fma_f32 v[6:7], v[6:7], v[42:43], v[38:39]
	global_store_dwordx4 v[34:35], v[4:7], off offset:1024 sc1 nt
	ds_read_b32 v4, v50 offset:536
	ds_read_b32 v5, v51 offset:536
	s_waitcnt lgkmcnt(1)
	v_readfirstlane_b32 s3, v4
	s_cmp_lt_i32 s3, 0
	s_waitcnt lgkmcnt(0)
	v_readfirstlane_b32 s2, v5
	s_waitcnt vmcnt(4)
	v_lshlrev_b32_e32 v38, 16, v52
	v_and_b32_e32 v39, 0xffff0000, v52
	v_lshlrev_b32_e32 v40, 16, v53
	v_and_b32_e32 v41, 0xffff0000, v53
	s_cbranch_scc1 .LBB0_3905
	s_and_b64 vcc, exec, s[0:1]
	s_cbranch_vccnz .LBB0_3905
	s_mul_i32 s5, s9, s3
	s_mul_hi_u32 s24, s8, s3
	s_add_i32 s5, s24, s5
	s_mul_i32 s3, s8, s3
	s_lshl_b32 s24, s14, 2
	s_add_u32 s24, s3, s24
	s_addc_u32 s25, s5, 0
	v_lshl_add_u64 v[4:5], v[18:19], 0, s[24:25]
	s_mov_b32 s3, s6

.LBB0_3909:
	v_add_co_u32_e32 v4, vcc, 0x1000, v24
	global_load_dwordx2 v[52:53], v[28:29], off offset:3584
	global_load_dwordx2 v[48:49], v[30:31], off offset:3584
	global_load_dwordx2 v[42:43], v[26:27], off offset:3584
	v_addc_co_u32_e32 v5, vcc, 0, v25, vcc
	global_load_dwordx4 v[4:7], v[4:5], off offset:3072
	v_mov_b32_e32 v28, v22
	v_mov_b32_e32 v29, v22
	s_waitcnt vmcnt(6)
	v_lshlrev_b32_e32 v24, 16, v36
	v_and_b32_e32 v25, 0xffff0000, v36
	v_lshlrev_b32_e32 v26, 16, v37
	v_and_b32_e32 v27, 0xffff0000, v37
	v_pk_mul_f32 v[30:31], v[22:23], v[46:47]
	v_mov_b32_e32 v36, v20
	v_mov_b32_e32 v37, v20
	v_pk_mul_f32 v[28:29], v[28:29], v[44:45]
	v_pk_fma_f32 v[30:31], v[20:21], v[38:39], v[30:31]
	v_pk_fma_f32 v[28:29], v[36:37], v[40:41], v[28:29]
	s_waitcnt vmcnt(5)
	v_pk_fma_f32 v[0:1], v[0:1], v[30:31], v[24:25]
	v_pk_fma_f32 v[2:3], v[2:3], v[28:29], v[26:27]
	global_store_dwordx4 v[34:35], v[0:3], off offset:2048 sc1 nt
	ds_read_b32 v0, v50 offset:540
	ds_read_b32 v24, v51 offset:540
	s_waitcnt lgkmcnt(1)
	v_readfirstlane_b32 s3, v0
	s_cmp_lt_i32 s3, 0
	s_waitcnt lgkmcnt(0)
	v_readfirstlane_b32 s2, v24
	s_waitcnt vmcnt(4)
	v_lshlrev_b32_e32 v0, 16, v52
	v_and_b32_e32 v1, 0xffff0000, v52
	v_lshlrev_b32_e32 v2, 16, v53
	v_and_b32_e32 v3, 0xffff0000, v53
	s_cbranch_scc1 .LBB0_3913
	s_and_b64 vcc, exec, s[0:1]
	s_cbranch_vccnz .LBB0_3913
	s_mul_i32 s5, s9, s3
	s_mul_hi_u32 s24, s8, s3
	s_add_i32 s5, s24, s5
	s_mul_i32 s3, s8, s3
	s_lshl_b32 s14, s14, 2
	s_add_u32 s24, s3, s14
	s_addc_u32 s25, s5, 0
	v_lshl_add_u64 v[24:25], v[18:19], 0, s[24:25]
	s_mov_b32 s3, s6
